# + nt on P10 Y-row loads and on the P6/P16 converters' fp8 stores
# speedup vs baseline: 1.0241x; 1.0184x over previous
; __device__ __forceinline__ unsigned pk4_fp8(float a, float b, float c, float d) { unsigned w = 0u; w = __builtin_amdgcn_cvt_pk_fp8_f32(a, b, w, false); w = __builtin_amdgcn_cvt_pk_fp8_f32(c, d, w, true); return w; }
; #define LAS __attribute__((address_space(3)))
; #define LDS_WAIT() asm volatile("s_waitcnt lgkmcnt(0)" ::: "memory")
; __device__ __forceinline__ void cvt_pack8(const f32x4 (&v)[16], const CvtItem& c, LAS unsigned char* blk, int s4, int lane) {
;     const float w = c.wscale; const int cb = lane & 15, j = 4 * s4 + (lane >> 4);
; #pragma unroll
;     for (int jn = 0; jn < 4; ++jn) {
;         v4u o; o.x = pg8::pk4_fp8(v[0][jn] * w, v[1][jn] * w, v[2][jn] * w, v[3][jn] * w); o.y = pg8::pk4_fp8(v[4][jn] * w, v[5][jn] * w, v[6][jn] * w, v[7][jn] * w);
;         o.z = pg8::pk4_fp8(v[8][jn] * w, v[9][jn] * w, v[10][jn] * w, v[11][jn] * w); o.w = pg8::pk4_fp8(v[12][jn] * w, v[13][jn] * w, v[14][jn] * w, v[15][jn] * w);
;         *(LAS v4u*)(blk + (4 * cb + jn) * 256 + ((j ^ cb) * 16)) = o; }
; }
; __device__ __forceinline__ void cvt_flush8(const CvtItem& c, const LAS unsigned char* blk, int lane) {
;     LDS_WAIT();
; #pragma unroll
;     for (int t = 0; t < 16; ++t) { const int idx = 64 * t + lane, n = idx >> 4, pc = idx & 15, nn = c.nb * 64 + n;
;         const size_t row = (c.which < 2) ? (size_t)((nn >> 7) * 256 + (nn & 127) + c.which * 128) : (size_t)nn;
;         *(v4u*)(c.dst + row * c.K + 16 * pc) = *(const LAS v4u*)(blk + n * 256 + ((pc ^ ((n >> 2) & 15)) * 16)); }
;     LDS_WAIT();
.LBB0_110:
	s_waitcnt vmcnt(15)
	v_mul_f32_e32 v110, v195, v110
	s_waitcnt vmcnt(14)
	v_mul_f32_e32 v118, v195, v118
	v_mov_b32_e32 v198, v131
	s_waitcnt vmcnt(11)
	v_mul_f32_e32 v98, v195, v98
	s_waitcnt vmcnt(10)
	v_mul_f32_e32 v102, v195, v102
	v_mov_b32_e32 v199, v131
	s_waitcnt vmcnt(7)
	v_mul_f32_e32 v78, v195, v78
	s_waitcnt vmcnt(6)
	v_mul_f32_e32 v86, v195, v86
	v_mov_b32_e32 v200, v131
	s_waitcnt vmcnt(3)
	v_mul_f32_e32 v66, v195, v66
	s_waitcnt vmcnt(2)
	v_mul_f32_e32 v70, v195, v70
	v_mov_b32_e32 v201, v131
	v_cvt_pk_fp8_f32 v198, v110, v118
	v_cvt_pk_fp8_f32 v199, v98, v102
	v_cvt_pk_fp8_f32 v200, v78, v86
	v_cvt_pk_fp8_f32 v201, v66, v70
	v_mul_f32_e32 v122, v195, v122
	v_mul_f32_e32 v126, v195, v126
	v_mul_f32_e32 v106, v195, v106
	v_mul_f32_e32 v110, v195, v114
	v_mul_f32_e32 v90, v195, v90
	v_mul_f32_e32 v94, v195, v94
	s_waitcnt vmcnt(1)
	v_mul_f32_e32 v74, v195, v74
	s_waitcnt vmcnt(0)
	v_mul_f32_e32 v78, v195, v82
	v_cvt_pk_fp8_f32 v198, v122, v126 op_sel:[0,0,1]
	v_cvt_pk_fp8_f32 v199, v106, v110 op_sel:[0,0,1]
	v_cvt_pk_fp8_f32 v200, v90, v94 op_sel:[0,0,1]
	v_cvt_pk_fp8_f32 v201, v74, v78 op_sel:[0,0,1]
	v_mul_f32_e32 v66, v195, v111
	v_mul_f32_e32 v70, v195, v119
	v_mul_f32_e32 v74, v195, v123
	ds_write_b128 v159, v[198:201]
	v_mov_b32_e32 v198, v131
	v_cvt_pk_fp8_f32 v198, v66, v70
	v_mul_f32_e32 v66, v195, v99
	v_mul_f32_e32 v70, v195, v103
	v_mov_b32_e32 v199, v131
	v_cvt_pk_fp8_f32 v199, v66, v70
	v_mul_f32_e32 v66, v195, v79
	v_mul_f32_e32 v70, v195, v87
	v_mov_b32_e32 v200, v131
	v_cvt_pk_fp8_f32 v200, v66, v70
	v_mul_f32_e32 v66, v195, v67
	v_mul_f32_e32 v67, v195, v71
	v_mov_b32_e32 v201, v131
	v_cvt_pk_fp8_f32 v201, v66, v67
	v_mul_f32_e32 v78, v195, v127
	v_cvt_pk_fp8_f32 v198, v74, v78 op_sel:[0,0,1]
	v_mul_f32_e32 v74, v195, v107
	v_mul_f32_e32 v78, v195, v115
	v_cvt_pk_fp8_f32 v199, v74, v78 op_sel:[0,0,1]
	v_mul_f32_e32 v74, v195, v91
	v_mul_f32_e32 v78, v195, v95
	v_mul_f32_e32 v70, v195, v75
	v_mul_f32_e32 v71, v195, v83
	v_cvt_pk_fp8_f32 v200, v74, v78 op_sel:[0,0,1]
	v_cvt_pk_fp8_f32 v201, v70, v71 op_sel:[0,0,1]
	v_mul_f32_e32 v66, v195, v112
	v_mul_f32_e32 v67, v195, v120
	v_mul_f32_e32 v70, v195, v124
	ds_write_b128 v159, v[198:201] offset:256
	v_mov_b32_e32 v198, v131
	v_cvt_pk_fp8_f32 v198, v66, v67
	v_mul_f32_e32 v66, v195, v100
	v_mul_f32_e32 v67, v195, v104
	v_mov_b32_e32 v199, v131
	v_cvt_pk_fp8_f32 v199, v66, v67
	v_mul_f32_e32 v66, v195, v80
	v_mul_f32_e32 v67, v195, v88
	v_mov_b32_e32 v200, v131
	v_cvt_pk_fp8_f32 v200, v66, v67
	v_mul_f32_e32 v66, v195, v68
	v_mul_f32_e32 v67, v195, v72
	v_mov_b32_e32 v201, v131
	v_mul_f32_e32 v71, v195, v128
	v_cvt_pk_fp8_f32 v201, v66, v67
	v_cvt_pk_fp8_f32 v198, v70, v71 op_sel:[0,0,1]
	v_mul_f32_e32 v70, v195, v108
	v_mul_f32_e32 v71, v195, v116
	v_cvt_pk_fp8_f32 v199, v70, v71 op_sel:[0,0,1]
	v_mul_f32_e32 v70, v195, v92
	v_mul_f32_e32 v71, v195, v96
	v_cvt_pk_fp8_f32 v200, v70, v71 op_sel:[0,0,1]
	v_mul_f32_e32 v68, v195, v76
	v_mul_f32_e32 v70, v195, v84
	v_cvt_pk_fp8_f32 v201, v68, v70 op_sel:[0,0,1]
	v_mul_f32_e32 v67, v195, v113
	v_mul_f32_e32 v68, v195, v121
	v_mov_b32_e32 v66, v131
	v_cvt_pk_fp8_f32 v66, v67, v68
	v_mul_f32_e32 v70, v195, v125
	v_mul_f32_e32 v71, v195, v129
	v_mul_f32_e32 v68, v195, v101
	v_cvt_pk_fp8_f32 v66, v70, v71 op_sel:[0,0,1]
	v_mul_f32_e32 v70, v195, v105
	v_mov_b32_e32 v67, v131
	v_cvt_pk_fp8_f32 v67, v68, v70
	v_mul_f32_e32 v71, v195, v109
	v_mul_f32_e32 v72, v195, v117
	v_mul_f32_e32 v70, v195, v81
	v_cvt_pk_fp8_f32 v67, v71, v72 op_sel:[0,0,1]
	v_mul_f32_e32 v71, v195, v89
	v_mov_b32_e32 v68, v131
	v_cvt_pk_fp8_f32 v68, v70, v71
	v_mul_f32_e32 v70, v195, v69
	v_mul_f32_e32 v71, v195, v73
	v_mov_b32_e32 v69, v131
	v_cvt_pk_fp8_f32 v69, v70, v71
	v_mul_f32_e32 v72, v195, v93
	v_mul_f32_e32 v74, v195, v97
	v_cvt_pk_fp8_f32 v68, v72, v74 op_sel:[0,0,1]
	v_mul_f32_e32 v72, v195, v77
	v_mul_f32_e32 v73, v195, v85
	v_cvt_pk_fp8_f32 v69, v72, v73 op_sel:[0,0,1]
	s_lshl_b32 s0, s39, 6
	s_cmp_lt_i32 s40, 2
	ds_write_b128 v159, v[198:201] offset:512
	ds_write_b128 v159, v[66:69] offset:768
	s_cselect_b64 vcc, -1, 0
	s_and_b32 s1, s39, 0x1fffffe
	s_waitcnt lgkmcnt(0)
	s_add_i32 s1, s1, s40
	v_bitop3_b32 v67, s0, v179, v140 bitop3:0xc8
	s_lshl_b32 s1, s1, 7
	ds_read_b128 v[68:71], v160
	v_or_b32_e32 v66, s0, v140
	v_or_b32_e32 v67, s1, v67
	v_cndmask_b32_e32 v72, v66, v67, vcc
	v_mov_b64_e32 v[66:67], s[10:11]
	v_mad_i64_i32 v[72:73], s[10:11], v72, s37, v[66:67]
	v_lshl_add_u64 v[72:73], v[72:73], 0, v[132:133]
	s_waitcnt lgkmcnt(0)
	global_store_dwordx4 v[72:73], v[68:71], off nt
	s_add_i32 s41, s41, s42
	s_add_i32 s43, s43, s44
	v_bitop3_b32 v69, s0, v180, v141 bitop3:0xc8
	v_or_b32_e32 v68, s0, v141
	v_or_b32_e32 v69, s1, v69
	v_cndmask_b32_e32 v72, v68, v69, vcc
	ds_read_b128 v[68:71], v161
	v_mad_i64_i32 v[72:73], s[10:11], v72, s37, v[66:67]
	v_lshl_add_u64 v[72:73], v[72:73], 0, v[132:133]
	s_mov_b32 s40, s46
	s_waitcnt lgkmcnt(0)
; #define LAS __attribute__((address_space(3)))
; #define LDS_WAIT() asm volatile("s_waitcnt lgkmcnt(0)" ::: "memory")
; __device__ __forceinline__ void cvt_flush8(const CvtItem& c, const LAS unsigned char* blk, int lane) {
;     LDS_WAIT();
; #pragma unroll
;     for (int t = 0; t < 16; ++t) { const int idx = 64 * t + lane, n = idx >> 4, pc = idx & 15, nn = c.nb * 64 + n;
;         const size_t row = (c.which < 2) ? (size_t)((nn >> 7) * 256 + (nn & 127) + c.which * 128) : (size_t)nn;
;         *(v4u*)(c.dst + row * c.K + 16 * pc) = *(const LAS v4u*)(blk + n * 256 + ((pc ^ ((n >> 2) & 15)) * 16)); }
;     LDS_WAIT();
	global_store_dwordx4 v[72:73], v[68:71], off nt
	s_mov_b32 s39, s45
	v_mov_b32_e32 v195, v196
	v_bitop3_b32 v69, s0, v181, v142 bitop3:0xc8
	v_or_b32_e32 v68, s0, v142
	v_or_b32_e32 v69, s1, v69
	v_cndmask_b32_e32 v72, v68, v69, vcc
	ds_read_b128 v[68:71], v162
	v_mad_i64_i32 v[72:73], s[10:11], v72, s37, v[66:67]
	v_lshl_add_u64 v[72:73], v[72:73], 0, v[132:133]
	s_waitcnt lgkmcnt(0)
	global_store_dwordx4 v[72:73], v[68:71], off nt
	s_nop 1
	v_bitop3_b32 v69, s0, v182, v143 bitop3:0xc8
	v_or_b32_e32 v68, s0, v143
	v_or_b32_e32 v69, s1, v69
	v_cndmask_b32_e32 v72, v68, v69, vcc
	ds_read_b128 v[68:71], v163
	v_mad_i64_i32 v[72:73], s[10:11], v72, s37, v[66:67]
	v_lshl_add_u64 v[72:73], v[72:73], 0, v[132:133]
	s_waitcnt lgkmcnt(0)
	global_store_dwordx4 v[72:73], v[68:71], off nt
	s_nop 1
	v_bitop3_b32 v69, s0, v183, v144 bitop3:0xc8
	v_or_b32_e32 v68, s0, v144
	v_or_b32_e32 v69, s1, v69
	v_cndmask_b32_e32 v72, v68, v69, vcc
	ds_read_b128 v[68:71], v164
	v_mad_i64_i32 v[72:73], s[10:11], v72, s37, v[66:67]
	v_lshl_add_u64 v[72:73], v[72:73], 0, v[132:133]
	s_waitcnt lgkmcnt(0)
	global_store_dwordx4 v[72:73], v[68:71], off nt
	s_nop 1
	v_bitop3_b32 v69, s0, v184, v145 bitop3:0xc8
	v_or_b32_e32 v68, s0, v145
	v_or_b32_e32 v69, s1, v69
	v_cndmask_b32_e32 v72, v68, v69, vcc
	ds_read_b128 v[68:71], v165
	v_mad_i64_i32 v[72:73], s[10:11], v72, s37, v[66:67]
	v_lshl_add_u64 v[72:73], v[72:73], 0, v[132:133]
	s_waitcnt lgkmcnt(0)
	global_store_dwordx4 v[72:73], v[68:71], off nt
	s_nop 1
	v_bitop3_b32 v69, s0, v185, v146 bitop3:0xc8
	v_or_b32_e32 v68, s0, v146
	v_or_b32_e32 v69, s1, v69
	v_cndmask_b32_e32 v72, v68, v69, vcc
	ds_read_b128 v[68:71], v166
	v_mad_i64_i32 v[72:73], s[10:11], v72, s37, v[66:67]
	v_lshl_add_u64 v[72:73], v[72:73], 0, v[132:133]
	s_waitcnt lgkmcnt(0)
	global_store_dwordx4 v[72:73], v[68:71], off nt
	s_nop 1
	v_bitop3_b32 v69, s0, v186, v147 bitop3:0xc8
	v_or_b32_e32 v68, s0, v147
	v_or_b32_e32 v69, s1, v69
	v_cndmask_b32_e32 v72, v68, v69, vcc
	ds_read_b128 v[68:71], v167
	v_mad_i64_i32 v[72:73], s[10:11], v72, s37, v[66:67]
	v_lshl_add_u64 v[72:73], v[72:73], 0, v[132:133]
	s_waitcnt lgkmcnt(0)
	global_store_dwordx4 v[72:73], v[68:71], off nt
	s_nop 1
	v_bitop3_b32 v69, s0, v187, v148 bitop3:0xc8
	v_or_b32_e32 v68, s0, v148
	v_or_b32_e32 v69, s1, v69
	v_cndmask_b32_e32 v72, v68, v69, vcc
	ds_read_b128 v[68:71], v168
	v_mad_i64_i32 v[72:73], s[10:11], v72, s37, v[66:67]
	v_lshl_add_u64 v[72:73], v[72:73], 0, v[132:133]
	s_waitcnt lgkmcnt(0)
	global_store_dwordx4 v[72:73], v[68:71], off nt
	s_nop 1
	v_bitop3_b32 v69, s0, v188, v149 bitop3:0xc8
	v_or_b32_e32 v68, s0, v149
	v_or_b32_e32 v69, s1, v69
	v_cndmask_b32_e32 v72, v68, v69, vcc
	ds_read_b128 v[68:71], v169
	v_mad_i64_i32 v[72:73], s[10:11], v72, s37, v[66:67]
	v_lshl_add_u64 v[72:73], v[72:73], 0, v[132:133]
	s_waitcnt lgkmcnt(0)
	global_store_dwordx4 v[72:73], v[68:71], off nt
	s_nop 1
	v_bitop3_b32 v69, s0, v189, v150 bitop3:0xc8
	v_or_b32_e32 v68, s0, v150
	v_or_b32_e32 v69, s1, v69
	v_cndmask_b32_e32 v72, v68, v69, vcc
	ds_read_b128 v[68:71], v170
	v_mad_i64_i32 v[72:73], s[10:11], v72, s37, v[66:67]
	v_lshl_add_u64 v[72:73], v[72:73], 0, v[132:133]
	s_waitcnt lgkmcnt(0)
	global_store_dwordx4 v[72:73], v[68:71], off nt
	s_nop 1
	v_bitop3_b32 v69, s0, v190, v151 bitop3:0xc8
	v_or_b32_e32 v68, s0, v151
	v_or_b32_e32 v69, s1, v69
	v_cndmask_b32_e32 v72, v68, v69, vcc
	ds_read_b128 v[68:71], v171
	v_mad_i64_i32 v[72:73], s[10:11], v72, s37, v[66:67]
	v_lshl_add_u64 v[72:73], v[72:73], 0, v[132:133]
	s_waitcnt lgkmcnt(0)
	global_store_dwordx4 v[72:73], v[68:71], off nt
	s_nop 1
	v_bitop3_b32 v69, s0, v191, v152 bitop3:0xc8
	v_or_b32_e32 v68, s0, v152
	v_or_b32_e32 v69, s1, v69
	v_cndmask_b32_e32 v72, v68, v69, vcc
	ds_read_b128 v[68:71], v172
	v_mad_i64_i32 v[72:73], s[10:11], v72, s37, v[66:67]
	v_lshl_add_u64 v[72:73], v[72:73], 0, v[132:133]
	s_waitcnt lgkmcnt(0)
	global_store_dwordx4 v[72:73], v[68:71], off nt
	s_nop 1
	v_bitop3_b32 v69, s0, v192, v153 bitop3:0xc8
	v_or_b32_e32 v68, s0, v153
	v_or_b32_e32 v69, s1, v69
	v_cndmask_b32_e32 v72, v68, v69, vcc
	ds_read_b128 v[68:71], v173
	v_mad_i64_i32 v[72:73], s[10:11], v72, s37, v[66:67]
	v_lshl_add_u64 v[72:73], v[72:73], 0, v[132:133]
	s_waitcnt lgkmcnt(0)
	global_store_dwordx4 v[72:73], v[68:71], off nt
	s_nop 1
	v_bitop3_b32 v69, s0, v193, v154 bitop3:0xc8
	v_or_b32_e32 v68, s0, v154
	v_or_b32_e32 v69, s1, v69
	v_cndmask_b32_e32 v72, v68, v69, vcc
	ds_read_b128 v[68:71], v174
	v_mad_i64_i32 v[72:73], s[10:11], v72, s37, v[66:67]
	v_lshl_add_u64 v[72:73], v[72:73], 0, v[132:133]
	s_mov_b64 s[10:11], s[22:23]
	s_waitcnt lgkmcnt(0)
	global_store_dwordx4 v[72:73], v[68:71], off nt
	s_nop 1
	v_bitop3_b32 v69, s0, v194, v155 bitop3:0xc8
	v_or_b32_e32 v68, s0, v155
	v_or_b32_e32 v69, s1, v69
	v_cndmask_b32_e32 v72, v68, v69, vcc
	ds_read_b128 v[68:71], v175
	v_mad_i64_i32 v[66:67], s[0:1], v72, s37, v[66:67]
	v_lshl_add_u64 v[66:67], v[66:67], 0, v[132:133]
	s_andn2_b64 vcc, exec, s[24:25]
	s_waitcnt lgkmcnt(0)
	global_store_dwordx4 v[66:67], v[68:71], off nt
	s_waitcnt lgkmcnt(0)
	s_mov_b32 s37, s47
	s_cbranch_vccz .LBB0_123

; __device__ __forceinline__ void topk_phase(const float* AFF, int* IDX, float* GATE, int* SEL, LAS unsigned* sc, int G, int blk, int tid, int lane, int wave) {
;     ...
;         v4i* so = (v4i*)(SEL + ((size_t)b * NE + e) * SEQ) + 4 * tid;
; #pragma unroll
;         for (int j = 0; j < 4; ++j) so[j] = (v4i){sl[4 * j], sl[4 * j + 1], sl[4 * j + 2], sl[4 * j + 3]};
;         __syncthreads();
.LBB0_593:
	s_or_b64 exec, exec, s[20:21]
	s_ashr_i32 s20, s94, 2
	s_lshl_b32 s21, s94, 4
	s_and_b32 s21, s21, 48
	s_ashr_i32 s22, s20, 31
	s_add_u32 s20, s21, s20
	s_addc_u32 s21, 0, s22
	s_lshl_b64 s[20:21], s[20:21], 15
	v_lshl_add_u64 v[2:3], v[24:25], 0, s[20:21]
	v_readlane_b32 s20, v254, 9
	s_add_i32 s94, s94, s20
	s_cmp_lt_i32 s94, 64
	global_store_dwordx4 v[2:3], v[18:21], off nt
	global_store_dwordx4 v[2:3], v[14:17], off offset:16 nt
	global_store_dwordx4 v[2:3], v[10:13], off offset:32 nt
	global_store_dwordx4 v[2:3], v[6:9], off offset:48 nt
	s_barrier
	s_cbranch_scc0 .LBB0_713

; __device__ __forceinline__ unsigned pk4_fp8(float a, float b, float c, float d) { unsigned w = 0u; w = __builtin_amdgcn_cvt_pk_fp8_f32(a, b, w, false); w = __builtin_amdgcn_cvt_pk_fp8_f32(c, d, w, true); return w; }
; #define LAS __attribute__((address_space(3)))
; #define LDS_WAIT() asm volatile("s_waitcnt lgkmcnt(0)" ::: "memory")
; __device__ __forceinline__ void cvt_pack8(const f32x4 (&v)[16], const CvtItem& c, LAS unsigned char* blk, int s4, int lane) {
;     const float w = c.wscale; const int cb = lane & 15, j = 4 * s4 + (lane >> 4);
; #pragma unroll
;     for (int jn = 0; jn < 4; ++jn) {
;         v4u o; o.x = pg8::pk4_fp8(v[0][jn] * w, v[1][jn] * w, v[2][jn] * w, v[3][jn] * w); o.y = pg8::pk4_fp8(v[4][jn] * w, v[5][jn] * w, v[6][jn] * w, v[7][jn] * w);
;         o.z = pg8::pk4_fp8(v[8][jn] * w, v[9][jn] * w, v[10][jn] * w, v[11][jn] * w); o.w = pg8::pk4_fp8(v[12][jn] * w, v[13][jn] * w, v[14][jn] * w, v[15][jn] * w);
;         *(LAS v4u*)(blk + (4 * cb + jn) * 256 + ((j ^ cb) * 16)) = o; }
; }
; __device__ __forceinline__ void cvt_flush8(const CvtItem& c, const LAS unsigned char* blk, int lane) {
;     LDS_WAIT();
; #pragma unroll
;     for (int t = 0; t < 16; ++t) { const int idx = 64 * t + lane, n = idx >> 4, pc = idx & 15, nn = c.nb * 64 + n;
;         const size_t row = (c.which < 2) ? (size_t)((nn >> 7) * 256 + (nn & 127) + c.which * 128) : (size_t)nn;
;         *(v4u*)(c.dst + row * c.K + 16 * pc) = *(const LAS v4u*)(blk + n * 256 + ((pc ^ ((n >> 2) & 15)) * 16)); }
;     LDS_WAIT();
.LBB0_717:
	s_waitcnt vmcnt(7)
	v_mul_f32_e32 v66, v179, v66
	s_waitcnt vmcnt(6)
	v_mul_f32_e32 v70, v179, v70
	v_mov_b32_e32 v180, 0
	v_cvt_pk_fp8_f32 v180, v66, v70
	v_mul_f32_e32 v66, v179, v78
	v_mul_f32_e32 v70, v179, v90
	v_mov_b32_e32 v181, 0
	v_cvt_pk_fp8_f32 v181, v66, v70
	s_waitcnt vmcnt(5)
	v_mul_f32_e32 v66, v179, v86
	s_waitcnt vmcnt(4)
	v_mul_f32_e32 v70, v179, v98
	v_mov_b32_e32 v182, 0
	v_cvt_pk_fp8_f32 v182, v66, v70
	s_waitcnt vmcnt(3)
	v_mul_f32_e32 v66, v179, v110
	s_waitcnt vmcnt(2)
	v_mul_f32_e32 v70, v179, v118
	v_mov_b32_e32 v183, 0
	v_mul_f32_e32 v74, v179, v74
	v_mul_f32_e32 v82, v179, v82
	v_cvt_pk_fp8_f32 v183, v66, v70
	v_cvt_pk_fp8_f32 v180, v74, v82 op_sel:[0,0,1]
	v_mul_f32_e32 v74, v179, v94
	v_mul_f32_e32 v78, v179, v106
	v_cvt_pk_fp8_f32 v181, v74, v78 op_sel:[0,0,1]
	v_mul_f32_e32 v74, v179, v102
	v_mul_f32_e32 v78, v179, v114
	v_cvt_pk_fp8_f32 v182, v74, v78 op_sel:[0,0,1]
	s_waitcnt vmcnt(1)
	v_mul_f32_e32 v74, v179, v122
	s_waitcnt vmcnt(0)
	v_mul_f32_e32 v78, v179, v126
	v_cvt_pk_fp8_f32 v183, v74, v78 op_sel:[0,0,1]
	v_mul_f32_e32 v66, v179, v67
	v_mul_f32_e32 v67, v179, v71
	v_mul_f32_e32 v70, v179, v75
	ds_write_b128 v161, v[180:183]
	v_mov_b32_e32 v180, 0
	v_cvt_pk_fp8_f32 v180, v66, v67
	v_mul_f32_e32 v66, v179, v79
	v_mul_f32_e32 v67, v179, v91
	v_mov_b32_e32 v181, 0
	v_cvt_pk_fp8_f32 v181, v66, v67
	v_mul_f32_e32 v66, v179, v87
	v_mul_f32_e32 v67, v179, v99
	v_mov_b32_e32 v182, 0
	v_cvt_pk_fp8_f32 v182, v66, v67
	v_mul_f32_e32 v66, v179, v111
	v_mul_f32_e32 v67, v179, v119
	v_mov_b32_e32 v183, 0
	v_mul_f32_e32 v71, v179, v83
	v_cvt_pk_fp8_f32 v183, v66, v67
	v_cvt_pk_fp8_f32 v180, v70, v71 op_sel:[0,0,1]
	v_mul_f32_e32 v70, v179, v95
	v_mul_f32_e32 v71, v179, v107
	v_cvt_pk_fp8_f32 v181, v70, v71 op_sel:[0,0,1]
	v_mul_f32_e32 v70, v179, v103
	v_mul_f32_e32 v71, v179, v115
	v_cvt_pk_fp8_f32 v182, v70, v71 op_sel:[0,0,1]
	v_mul_f32_e32 v70, v179, v123
	v_mul_f32_e32 v71, v179, v127
	v_cvt_pk_fp8_f32 v183, v70, v71 op_sel:[0,0,1]
	v_mul_f32_e32 v66, v179, v68
	v_mul_f32_e32 v67, v179, v72
	v_mul_f32_e32 v68, v179, v76
	ds_write_b128 v161, v[180:183] offset:256
	v_mov_b32_e32 v180, 0
	v_cvt_pk_fp8_f32 v180, v66, v67
	v_mul_f32_e32 v66, v179, v80
	v_mul_f32_e32 v67, v179, v92
	v_mov_b32_e32 v181, 0
	v_cvt_pk_fp8_f32 v181, v66, v67
	v_mul_f32_e32 v66, v179, v88
	v_mul_f32_e32 v67, v179, v100
	v_mov_b32_e32 v182, 0
	v_cvt_pk_fp8_f32 v182, v66, v67
	v_mul_f32_e32 v66, v179, v112
	v_mul_f32_e32 v67, v179, v120
	v_mov_b32_e32 v183, 0
	v_mul_f32_e32 v70, v179, v84
	v_cvt_pk_fp8_f32 v183, v66, v67
	v_cvt_pk_fp8_f32 v180, v68, v70 op_sel:[0,0,1]
	v_mul_f32_e32 v68, v179, v96
	v_mul_f32_e32 v70, v179, v108
	v_cvt_pk_fp8_f32 v181, v68, v70 op_sel:[0,0,1]
	v_mul_f32_e32 v68, v179, v104
	v_mul_f32_e32 v70, v179, v116
	v_cvt_pk_fp8_f32 v182, v68, v70 op_sel:[0,0,1]
	v_mul_f32_e32 v68, v179, v124
	v_mul_f32_e32 v70, v179, v128
	v_cvt_pk_fp8_f32 v183, v68, v70 op_sel:[0,0,1]
	v_mul_f32_e32 v67, v179, v69
	v_mul_f32_e32 v68, v179, v73
	v_mov_b32_e32 v66, 0
	v_cvt_pk_fp8_f32 v66, v67, v68
	v_mul_f32_e32 v69, v179, v77
	v_mul_f32_e32 v70, v179, v85
	v_mul_f32_e32 v68, v179, v81
	v_cvt_pk_fp8_f32 v66, v69, v70 op_sel:[0,0,1]
	v_mul_f32_e32 v69, v179, v93
	v_mov_b32_e32 v67, 0
	v_cvt_pk_fp8_f32 v67, v68, v69
	v_mul_f32_e32 v70, v179, v97
	v_mul_f32_e32 v71, v179, v109
	v_mul_f32_e32 v69, v179, v89
	v_cvt_pk_fp8_f32 v67, v70, v71 op_sel:[0,0,1]
	v_mul_f32_e32 v70, v179, v101
	v_mov_b32_e32 v68, 0
	v_cvt_pk_fp8_f32 v68, v69, v70
	v_mul_f32_e32 v71, v179, v105
	v_mul_f32_e32 v72, v179, v117
	v_mul_f32_e32 v70, v179, v113
	v_cvt_pk_fp8_f32 v68, v71, v72 op_sel:[0,0,1]
	v_mul_f32_e32 v71, v179, v121
	v_mov_b32_e32 v69, 0
	v_cvt_pk_fp8_f32 v69, v70, v71
	v_mul_f32_e32 v72, v179, v125
	v_mul_f32_e32 v73, v179, v129
	s_lshl_b32 s4, s31, 6
	v_cvt_pk_fp8_f32 v69, v72, v73 op_sel:[0,0,1]
	s_and_b32 s31, s31, 0x1fffffe
	ds_write_b128 v161, v[180:183] offset:512
	s_and_b32 s4, s4, 64
	ds_write_b128 v161, v[66:69] offset:768
	s_add_i32 s31, s31, s30
	s_waitcnt lgkmcnt(0)
	v_or_b32_e32 v66, s4, v142
	s_lshl_b32 s30, s31, 7
	v_or_b32_e32 v70, s30, v66
	ds_read_b128 v[66:69], v162
	v_ashrrev_i32_e32 v71, 31, v70
	v_lshlrev_b64 v[70:71], 10, v[70:71]
	v_lshl_add_u64 v[70:71], s[6:7], 0, v[70:71]
	v_lshl_add_u64 v[70:71], v[70:71], 0, v[134:135]
	s_waitcnt lgkmcnt(0)
	global_store_dwordx4 v[70:71], v[66:69], off nt
	s_add_i32 s25, s25, s26
	s_andn2_b64 vcc, exec, s[2:3]
	v_or_b32_e32 v66, s4, v143
	v_or_b32_e32 v70, s30, v66
	ds_read_b128 v[66:69], v163
	v_ashrrev_i32_e32 v71, 31, v70
	v_lshlrev_b64 v[70:71], 10, v[70:71]
	v_lshl_add_u64 v[70:71], s[6:7], 0, v[70:71]
	v_lshl_add_u64 v[70:71], v[70:71], 0, v[134:135]
	s_waitcnt lgkmcnt(0)
; #define LAS __attribute__((address_space(3)))
; #define LDS_WAIT() asm volatile("s_waitcnt lgkmcnt(0)" ::: "memory")
; __device__ __forceinline__ void cvt_flush8(const CvtItem& c, const LAS unsigned char* blk, int lane) {
;     LDS_WAIT();
; #pragma unroll
;     for (int t = 0; t < 16; ++t) { const int idx = 64 * t + lane, n = idx >> 4, pc = idx & 15, nn = c.nb * 64 + n;
;         const size_t row = (c.which < 2) ? (size_t)((nn >> 7) * 256 + (nn & 127) + c.which * 128) : (size_t)nn;
;         *(v4u*)(c.dst + row * c.K + 16 * pc) = *(const LAS v4u*)(blk + n * 256 + ((pc ^ ((n >> 2) & 15)) * 16)); }
;     LDS_WAIT();
	global_store_dwordx4 v[70:71], v[66:69], off nt
	s_mov_b32 s31, s28
	v_mov_b32_e32 v179, v178
	v_or_b32_e32 v66, s4, v144
	v_or_b32_e32 v70, s30, v66
	ds_read_b128 v[66:69], v164
	v_ashrrev_i32_e32 v71, 31, v70
	v_lshlrev_b64 v[70:71], 10, v[70:71]
	v_lshl_add_u64 v[70:71], s[6:7], 0, v[70:71]
	v_lshl_add_u64 v[70:71], v[70:71], 0, v[134:135]
	s_waitcnt lgkmcnt(0)
	global_store_dwordx4 v[70:71], v[66:69], off nt
	s_nop 1
	v_or_b32_e32 v66, s4, v145
	v_or_b32_e32 v70, s30, v66
	ds_read_b128 v[66:69], v165
	v_ashrrev_i32_e32 v71, 31, v70
	v_lshlrev_b64 v[70:71], 10, v[70:71]
	v_lshl_add_u64 v[70:71], s[6:7], 0, v[70:71]
	v_lshl_add_u64 v[70:71], v[70:71], 0, v[134:135]
	s_waitcnt lgkmcnt(0)
	global_store_dwordx4 v[70:71], v[66:69], off nt
	s_nop 1
	v_or_b32_e32 v66, s4, v146
	v_or_b32_e32 v70, s30, v66
	ds_read_b128 v[66:69], v166
	v_ashrrev_i32_e32 v71, 31, v70
	v_lshlrev_b64 v[70:71], 10, v[70:71]
	v_lshl_add_u64 v[70:71], s[6:7], 0, v[70:71]
	v_lshl_add_u64 v[70:71], v[70:71], 0, v[134:135]
	s_waitcnt lgkmcnt(0)
	global_store_dwordx4 v[70:71], v[66:69], off nt
	s_nop 1
	v_or_b32_e32 v66, s4, v147
	v_or_b32_e32 v70, s30, v66
	ds_read_b128 v[66:69], v167
	v_ashrrev_i32_e32 v71, 31, v70
	v_lshlrev_b64 v[70:71], 10, v[70:71]
	v_lshl_add_u64 v[70:71], s[6:7], 0, v[70:71]
	v_lshl_add_u64 v[70:71], v[70:71], 0, v[134:135]
	s_waitcnt lgkmcnt(0)
	global_store_dwordx4 v[70:71], v[66:69], off nt
	s_nop 1
	v_or_b32_e32 v66, s4, v148
	v_or_b32_e32 v70, s30, v66
	ds_read_b128 v[66:69], v168
	v_ashrrev_i32_e32 v71, 31, v70
	v_lshlrev_b64 v[70:71], 10, v[70:71]
	v_lshl_add_u64 v[70:71], s[6:7], 0, v[70:71]
	v_lshl_add_u64 v[70:71], v[70:71], 0, v[134:135]
	s_waitcnt lgkmcnt(0)
	global_store_dwordx4 v[70:71], v[66:69], off nt
	s_nop 1
	v_or_b32_e32 v66, s4, v149
	v_or_b32_e32 v70, s30, v66
	ds_read_b128 v[66:69], v169
	v_ashrrev_i32_e32 v71, 31, v70
	v_lshlrev_b64 v[70:71], 10, v[70:71]
	v_lshl_add_u64 v[70:71], s[6:7], 0, v[70:71]
	v_lshl_add_u64 v[70:71], v[70:71], 0, v[134:135]
	s_waitcnt lgkmcnt(0)
	global_store_dwordx4 v[70:71], v[66:69], off nt
	s_nop 1
	v_or_b32_e32 v66, s4, v150
	v_or_b32_e32 v70, s30, v66
	ds_read_b128 v[66:69], v170
	v_ashrrev_i32_e32 v71, 31, v70
	v_lshlrev_b64 v[70:71], 10, v[70:71]
	v_lshl_add_u64 v[70:71], s[6:7], 0, v[70:71]
	v_lshl_add_u64 v[70:71], v[70:71], 0, v[134:135]
	s_waitcnt lgkmcnt(0)
	global_store_dwordx4 v[70:71], v[66:69], off nt
	s_nop 1
	v_or_b32_e32 v66, s4, v151
	v_or_b32_e32 v70, s30, v66
	ds_read_b128 v[66:69], v171
	v_ashrrev_i32_e32 v71, 31, v70
	v_lshlrev_b64 v[70:71], 10, v[70:71]
	v_lshl_add_u64 v[70:71], s[6:7], 0, v[70:71]
	v_lshl_add_u64 v[70:71], v[70:71], 0, v[134:135]
	s_waitcnt lgkmcnt(0)
	global_store_dwordx4 v[70:71], v[66:69], off nt
	s_nop 1
	v_or_b32_e32 v66, s4, v152
	v_or_b32_e32 v70, s30, v66
	ds_read_b128 v[66:69], v172
	v_ashrrev_i32_e32 v71, 31, v70
	v_lshlrev_b64 v[70:71], 10, v[70:71]
	v_lshl_add_u64 v[70:71], s[6:7], 0, v[70:71]
	v_lshl_add_u64 v[70:71], v[70:71], 0, v[134:135]
	s_waitcnt lgkmcnt(0)
	global_store_dwordx4 v[70:71], v[66:69], off nt
	s_nop 1
	v_or_b32_e32 v66, s4, v153
	v_or_b32_e32 v70, s30, v66
	ds_read_b128 v[66:69], v173
	v_ashrrev_i32_e32 v71, 31, v70
	v_lshlrev_b64 v[70:71], 10, v[70:71]
	v_lshl_add_u64 v[70:71], s[6:7], 0, v[70:71]
	v_lshl_add_u64 v[70:71], v[70:71], 0, v[134:135]
	s_waitcnt lgkmcnt(0)
	global_store_dwordx4 v[70:71], v[66:69], off nt
	s_nop 1
	v_or_b32_e32 v66, s4, v154
	v_or_b32_e32 v70, s30, v66
	ds_read_b128 v[66:69], v174
	v_ashrrev_i32_e32 v71, 31, v70
	v_lshlrev_b64 v[70:71], 10, v[70:71]
	v_lshl_add_u64 v[70:71], s[6:7], 0, v[70:71]
	v_lshl_add_u64 v[70:71], v[70:71], 0, v[134:135]
	s_waitcnt lgkmcnt(0)
	global_store_dwordx4 v[70:71], v[66:69], off nt
	s_nop 1
	v_or_b32_e32 v66, s4, v155
	v_or_b32_e32 v70, s30, v66
	ds_read_b128 v[66:69], v175
	v_ashrrev_i32_e32 v71, 31, v70
	v_lshlrev_b64 v[70:71], 10, v[70:71]
	v_lshl_add_u64 v[70:71], s[6:7], 0, v[70:71]
	v_lshl_add_u64 v[70:71], v[70:71], 0, v[134:135]
	s_waitcnt lgkmcnt(0)
	global_store_dwordx4 v[70:71], v[66:69], off nt
	s_nop 1
	v_or_b32_e32 v66, s4, v156
	v_or_b32_e32 v70, s30, v66
	ds_read_b128 v[66:69], v176
	v_ashrrev_i32_e32 v71, 31, v70
	v_lshlrev_b64 v[70:71], 10, v[70:71]
	v_lshl_add_u64 v[70:71], s[6:7], 0, v[70:71]
	v_lshl_add_u64 v[70:71], v[70:71], 0, v[134:135]
	s_waitcnt lgkmcnt(0)
	global_store_dwordx4 v[70:71], v[66:69], off nt
	s_nop 1
	v_or_b32_e32 v66, s4, v157
	v_or_b32_e32 v70, s30, v66
	ds_read_b128 v[66:69], v177
	v_ashrrev_i32_e32 v71, 31, v70
	v_lshlrev_b64 v[70:71], 10, v[70:71]
	v_lshl_add_u64 v[70:71], s[6:7], 0, v[70:71]
	v_lshl_add_u64 v[70:71], v[70:71], 0, v[134:135]
	s_waitcnt lgkmcnt(0)
	global_store_dwordx4 v[70:71], v[66:69], off nt
	s_waitcnt lgkmcnt(0)
	s_mov_b64 s[6:7], s[8:9]
	s_mov_b32 s30, s27
	s_cbranch_vccz .LBB0_720

; __device__ __forceinline__ unsigned pk4_fp8(float a, float b, float c, float d) { unsigned w = 0u; w = __builtin_amdgcn_cvt_pk_fp8_f32(a, b, w, false); w = __builtin_amdgcn_cvt_pk_fp8_f32(c, d, w, true); return w; }
; #define LAS __attribute__((address_space(3)))
; #define LDS_WAIT() asm volatile("s_waitcnt lgkmcnt(0)" ::: "memory")
; __device__ __forceinline__ void cvt_pack8(const f32x4 (&v)[16], const CvtItem& c, LAS unsigned char* blk, int s4, int lane) {
;     const float w = c.wscale; const int cb = lane & 15, j = 4 * s4 + (lane >> 4);
; #pragma unroll
;     for (int jn = 0; jn < 4; ++jn) {
;         v4u o; o.x = pg8::pk4_fp8(v[0][jn] * w, v[1][jn] * w, v[2][jn] * w, v[3][jn] * w); o.y = pg8::pk4_fp8(v[4][jn] * w, v[5][jn] * w, v[6][jn] * w, v[7][jn] * w);
;         o.z = pg8::pk4_fp8(v[8][jn] * w, v[9][jn] * w, v[10][jn] * w, v[11][jn] * w); o.w = pg8::pk4_fp8(v[12][jn] * w, v[13][jn] * w, v[14][jn] * w, v[15][jn] * w);
;         *(LAS v4u*)(blk + (4 * cb + jn) * 256 + ((j ^ cb) * 16)) = o; }
; }
; __device__ __forceinline__ void cvt_flush8(const CvtItem& c, const LAS unsigned char* blk, int lane) {
;     LDS_WAIT();
; #pragma unroll
;     for (int t = 0; t < 16; ++t) { const int idx = 64 * t + lane, n = idx >> 4, pc = idx & 15, nn = c.nb * 64 + n;
;         const size_t row = (c.which < 2) ? (size_t)((nn >> 7) * 256 + (nn & 127) + c.which * 128) : (size_t)nn;
;         *(v4u*)(c.dst + row * c.K + 16 * pc) = *(const LAS v4u*)(blk + n * 256 + ((pc ^ ((n >> 2) & 15)) * 16)); }
;     LDS_WAIT();
.LBB0_724:
	s_waitcnt vmcnt(7)
	v_mul_f32_e32 v66, v177, v66
	s_waitcnt vmcnt(6)
	v_mul_f32_e32 v70, v177, v70
	v_mov_b32_e32 v178, 0
	v_cvt_pk_fp8_f32 v178, v66, v70
	v_mul_f32_e32 v66, v177, v78
	v_mul_f32_e32 v70, v177, v90
	v_mov_b32_e32 v179, 0
	v_cvt_pk_fp8_f32 v179, v66, v70
	s_waitcnt vmcnt(5)
	v_mul_f32_e32 v66, v177, v86
	s_waitcnt vmcnt(4)
	v_mul_f32_e32 v70, v177, v98
	v_mov_b32_e32 v180, 0
	v_cvt_pk_fp8_f32 v180, v66, v70
	s_waitcnt vmcnt(3)
	v_mul_f32_e32 v66, v177, v110
	s_waitcnt vmcnt(2)
	v_mul_f32_e32 v70, v177, v118
	v_mov_b32_e32 v181, 0
	v_mul_f32_e32 v74, v177, v74
	v_mul_f32_e32 v82, v177, v82
	v_cvt_pk_fp8_f32 v181, v66, v70
	v_cvt_pk_fp8_f32 v178, v74, v82 op_sel:[0,0,1]
	v_mul_f32_e32 v74, v177, v94
	v_mul_f32_e32 v78, v177, v106
	v_cvt_pk_fp8_f32 v179, v74, v78 op_sel:[0,0,1]
	v_mul_f32_e32 v74, v177, v102
	v_mul_f32_e32 v78, v177, v114
	v_cvt_pk_fp8_f32 v180, v74, v78 op_sel:[0,0,1]
	s_waitcnt vmcnt(1)
	v_mul_f32_e32 v74, v177, v122
	s_waitcnt vmcnt(0)
	v_mul_f32_e32 v78, v177, v126
	v_cvt_pk_fp8_f32 v181, v74, v78 op_sel:[0,0,1]
	v_mul_f32_e32 v66, v177, v67
	v_mul_f32_e32 v67, v177, v71
	v_mul_f32_e32 v70, v177, v75
	ds_write_b128 v159, v[178:181]
	v_mov_b32_e32 v178, 0
	v_cvt_pk_fp8_f32 v178, v66, v67
	v_mul_f32_e32 v66, v177, v79
	v_mul_f32_e32 v67, v177, v91
	v_mov_b32_e32 v179, 0
	v_cvt_pk_fp8_f32 v179, v66, v67
	v_mul_f32_e32 v66, v177, v87
	v_mul_f32_e32 v67, v177, v99
	v_mov_b32_e32 v180, 0
	v_cvt_pk_fp8_f32 v180, v66, v67
	v_mul_f32_e32 v66, v177, v111
	v_mul_f32_e32 v67, v177, v119
	v_mov_b32_e32 v181, 0
	v_mul_f32_e32 v71, v177, v83
	v_cvt_pk_fp8_f32 v181, v66, v67
	v_cvt_pk_fp8_f32 v178, v70, v71 op_sel:[0,0,1]
	v_mul_f32_e32 v70, v177, v95
	v_mul_f32_e32 v71, v177, v107
	v_cvt_pk_fp8_f32 v179, v70, v71 op_sel:[0,0,1]
	v_mul_f32_e32 v70, v177, v103
	v_mul_f32_e32 v71, v177, v115
	v_cvt_pk_fp8_f32 v180, v70, v71 op_sel:[0,0,1]
	v_mul_f32_e32 v70, v177, v123
	v_mul_f32_e32 v71, v177, v127
	v_cvt_pk_fp8_f32 v181, v70, v71 op_sel:[0,0,1]
	v_mul_f32_e32 v66, v177, v68
	v_mul_f32_e32 v67, v177, v72
	v_mul_f32_e32 v68, v177, v76
	ds_write_b128 v159, v[178:181] offset:256
	v_mov_b32_e32 v178, 0
	v_cvt_pk_fp8_f32 v178, v66, v67
	v_mul_f32_e32 v66, v177, v80
	v_mul_f32_e32 v67, v177, v92
	v_mov_b32_e32 v179, 0
	v_cvt_pk_fp8_f32 v179, v66, v67
	v_mul_f32_e32 v66, v177, v88
	v_mul_f32_e32 v67, v177, v100
	v_mov_b32_e32 v180, 0
	v_cvt_pk_fp8_f32 v180, v66, v67
	v_mul_f32_e32 v66, v177, v112
	v_mul_f32_e32 v67, v177, v120
	v_mov_b32_e32 v181, 0
	v_mul_f32_e32 v70, v177, v84
	v_cvt_pk_fp8_f32 v181, v66, v67
	v_cvt_pk_fp8_f32 v178, v68, v70 op_sel:[0,0,1]
	v_mul_f32_e32 v68, v177, v96
	v_mul_f32_e32 v70, v177, v108
	v_cvt_pk_fp8_f32 v179, v68, v70 op_sel:[0,0,1]
	v_mul_f32_e32 v68, v177, v104
	v_mul_f32_e32 v70, v177, v116
	v_cvt_pk_fp8_f32 v180, v68, v70 op_sel:[0,0,1]
	v_mul_f32_e32 v68, v177, v124
	v_mul_f32_e32 v70, v177, v128
	v_cvt_pk_fp8_f32 v181, v68, v70 op_sel:[0,0,1]
	v_mul_f32_e32 v67, v177, v69
	v_mul_f32_e32 v68, v177, v73
	v_mov_b32_e32 v66, 0
	v_cvt_pk_fp8_f32 v66, v67, v68
	v_mul_f32_e32 v69, v177, v77
	v_mul_f32_e32 v70, v177, v85
	v_mul_f32_e32 v68, v177, v81
	v_cvt_pk_fp8_f32 v66, v69, v70 op_sel:[0,0,1]
	v_mul_f32_e32 v69, v177, v93
	v_mov_b32_e32 v67, 0
	v_cvt_pk_fp8_f32 v67, v68, v69
	v_mul_f32_e32 v70, v177, v97
	v_mul_f32_e32 v71, v177, v109
	v_mul_f32_e32 v69, v177, v89
	v_cvt_pk_fp8_f32 v67, v70, v71 op_sel:[0,0,1]
	v_mul_f32_e32 v70, v177, v101
	v_mov_b32_e32 v68, 0
	v_cvt_pk_fp8_f32 v68, v69, v70
	v_mul_f32_e32 v71, v177, v105
	v_mul_f32_e32 v72, v177, v117
	v_mul_f32_e32 v70, v177, v113
	v_cvt_pk_fp8_f32 v68, v71, v72 op_sel:[0,0,1]
	v_mul_f32_e32 v71, v177, v121
	v_mov_b32_e32 v69, 0
	v_cvt_pk_fp8_f32 v69, v70, v71
	v_mul_f32_e32 v72, v177, v125
	v_mul_f32_e32 v73, v177, v129
	s_lshl_b32 s4, s30, 6
	v_cvt_pk_fp8_f32 v69, v72, v73 op_sel:[0,0,1]
	s_and_b32 s30, s30, 0x1fffffe
	ds_write_b128 v159, v[178:181] offset:512
	s_and_b32 s4, s4, 64
	ds_write_b128 v159, v[66:69] offset:768
	s_add_i32 s30, s30, s29
	s_waitcnt lgkmcnt(0)
	v_or_b32_e32 v66, s4, v138
	s_lshl_b32 s29, s30, 7
	v_or_b32_e32 v70, s29, v66
	ds_read_b128 v[66:69], v160
	v_ashrrev_i32_e32 v71, 31, v70
	v_lshlrev_b64 v[70:71], 10, v[70:71]
	v_lshl_add_u64 v[70:71], s[6:7], 0, v[70:71]
	v_lshl_add_u64 v[70:71], v[70:71], 0, v[134:135]
	s_waitcnt lgkmcnt(0)
	global_store_dwordx4 v[70:71], v[66:69], off nt
	s_add_i32 s2, s2, s3
	s_add_i32 s25, s25, s26
	v_or_b32_e32 v66, s4, v1
	v_or_b32_e32 v70, s29, v66
	ds_read_b128 v[66:69], v161
	v_ashrrev_i32_e32 v71, 31, v70
	v_lshlrev_b64 v[70:71], 10, v[70:71]
	v_lshl_add_u64 v[70:71], s[6:7], 0, v[70:71]
	v_lshl_add_u64 v[70:71], v[70:71], 0, v[134:135]
	s_waitcnt lgkmcnt(0)
; #define LAS __attribute__((address_space(3)))
; #define LDS_WAIT() asm volatile("s_waitcnt lgkmcnt(0)" ::: "memory")
; __device__ __forceinline__ void cvt_flush8(const CvtItem& c, const LAS unsigned char* blk, int lane) {
;     LDS_WAIT();
; #pragma unroll
;     for (int t = 0; t < 16; ++t) { const int idx = 64 * t + lane, n = idx >> 4, pc = idx & 15, nn = c.nb * 64 + n;
;         const size_t row = (c.which < 2) ? (size_t)((nn >> 7) * 256 + (nn & 127) + c.which * 128) : (size_t)nn;
;         *(v4u*)(c.dst + row * c.K + 16 * pc) = *(const LAS v4u*)(blk + n * 256 + ((pc ^ ((n >> 2) & 15)) * 16)); }
;     LDS_WAIT();
	global_store_dwordx4 v[70:71], v[66:69], off nt
	s_cmpk_lt_i32 s2, 0x510
	s_mov_b32 s30, s28
	v_or_b32_e32 v66, s4, v142
	v_or_b32_e32 v70, s29, v66
	ds_read_b128 v[66:69], v162
	v_ashrrev_i32_e32 v71, 31, v70
	v_lshlrev_b64 v[70:71], 10, v[70:71]
	v_lshl_add_u64 v[70:71], s[6:7], 0, v[70:71]
	v_lshl_add_u64 v[70:71], v[70:71], 0, v[134:135]
	s_waitcnt lgkmcnt(0)
	global_store_dwordx4 v[70:71], v[66:69], off nt
	v_mov_b32_e32 v177, v176
	s_nop 0
	v_or_b32_e32 v66, s4, v143
	v_or_b32_e32 v70, s29, v66
	ds_read_b128 v[66:69], v163
	v_ashrrev_i32_e32 v71, 31, v70
	v_lshlrev_b64 v[70:71], 10, v[70:71]
	v_lshl_add_u64 v[70:71], s[6:7], 0, v[70:71]
	v_lshl_add_u64 v[70:71], v[70:71], 0, v[134:135]
	s_waitcnt lgkmcnt(0)
	global_store_dwordx4 v[70:71], v[66:69], off nt
	s_nop 1
	v_or_b32_e32 v66, s4, v144
	v_or_b32_e32 v70, s29, v66
	ds_read_b128 v[66:69], v164
	v_ashrrev_i32_e32 v71, 31, v70
	v_lshlrev_b64 v[70:71], 10, v[70:71]
	v_lshl_add_u64 v[70:71], s[6:7], 0, v[70:71]
	v_lshl_add_u64 v[70:71], v[70:71], 0, v[134:135]
	s_waitcnt lgkmcnt(0)
	global_store_dwordx4 v[70:71], v[66:69], off nt
	s_nop 1
	v_or_b32_e32 v66, s4, v145
	v_or_b32_e32 v70, s29, v66
	ds_read_b128 v[66:69], v165
	v_ashrrev_i32_e32 v71, 31, v70
	v_lshlrev_b64 v[70:71], 10, v[70:71]
	v_lshl_add_u64 v[70:71], s[6:7], 0, v[70:71]
	v_lshl_add_u64 v[70:71], v[70:71], 0, v[134:135]
	s_waitcnt lgkmcnt(0)
	global_store_dwordx4 v[70:71], v[66:69], off nt
	s_nop 1
	v_or_b32_e32 v66, s4, v146
	v_or_b32_e32 v70, s29, v66
	ds_read_b128 v[66:69], v166
	v_ashrrev_i32_e32 v71, 31, v70
	v_lshlrev_b64 v[70:71], 10, v[70:71]
	v_lshl_add_u64 v[70:71], s[6:7], 0, v[70:71]
	v_lshl_add_u64 v[70:71], v[70:71], 0, v[134:135]
	s_waitcnt lgkmcnt(0)
	global_store_dwordx4 v[70:71], v[66:69], off nt
	s_nop 1
	v_or_b32_e32 v66, s4, v147
	v_or_b32_e32 v70, s29, v66
	ds_read_b128 v[66:69], v167
	v_ashrrev_i32_e32 v71, 31, v70
	v_lshlrev_b64 v[70:71], 10, v[70:71]
	v_lshl_add_u64 v[70:71], s[6:7], 0, v[70:71]
	v_lshl_add_u64 v[70:71], v[70:71], 0, v[134:135]
	s_waitcnt lgkmcnt(0)
	global_store_dwordx4 v[70:71], v[66:69], off nt
	s_nop 1
	v_or_b32_e32 v66, s4, v148
	v_or_b32_e32 v70, s29, v66
	ds_read_b128 v[66:69], v168
	v_ashrrev_i32_e32 v71, 31, v70
	v_lshlrev_b64 v[70:71], 10, v[70:71]
	v_lshl_add_u64 v[70:71], s[6:7], 0, v[70:71]
	v_lshl_add_u64 v[70:71], v[70:71], 0, v[134:135]
	s_waitcnt lgkmcnt(0)
	global_store_dwordx4 v[70:71], v[66:69], off nt
	s_nop 1
	v_or_b32_e32 v66, s4, v149
	v_or_b32_e32 v70, s29, v66
	ds_read_b128 v[66:69], v169
	v_ashrrev_i32_e32 v71, 31, v70
	v_lshlrev_b64 v[70:71], 10, v[70:71]
	v_lshl_add_u64 v[70:71], s[6:7], 0, v[70:71]
	v_lshl_add_u64 v[70:71], v[70:71], 0, v[134:135]
	s_waitcnt lgkmcnt(0)
	global_store_dwordx4 v[70:71], v[66:69], off nt
	s_nop 1
	v_or_b32_e32 v66, s4, v150
	v_or_b32_e32 v70, s29, v66
	ds_read_b128 v[66:69], v170
	v_ashrrev_i32_e32 v71, 31, v70
	v_lshlrev_b64 v[70:71], 10, v[70:71]
	v_lshl_add_u64 v[70:71], s[6:7], 0, v[70:71]
	v_lshl_add_u64 v[70:71], v[70:71], 0, v[134:135]
	s_waitcnt lgkmcnt(0)
	global_store_dwordx4 v[70:71], v[66:69], off nt
	s_nop 1
	v_or_b32_e32 v66, s4, v151
	v_or_b32_e32 v70, s29, v66
	ds_read_b128 v[66:69], v171
	v_ashrrev_i32_e32 v71, 31, v70
	v_lshlrev_b64 v[70:71], 10, v[70:71]
	v_lshl_add_u64 v[70:71], s[6:7], 0, v[70:71]
	v_lshl_add_u64 v[70:71], v[70:71], 0, v[134:135]
	s_waitcnt lgkmcnt(0)
	global_store_dwordx4 v[70:71], v[66:69], off nt
	s_nop 1
	v_or_b32_e32 v66, s4, v152
	v_or_b32_e32 v70, s29, v66
	ds_read_b128 v[66:69], v172
	v_ashrrev_i32_e32 v71, 31, v70
	v_lshlrev_b64 v[70:71], 10, v[70:71]
	v_lshl_add_u64 v[70:71], s[6:7], 0, v[70:71]
	v_lshl_add_u64 v[70:71], v[70:71], 0, v[134:135]
	s_waitcnt lgkmcnt(0)
	global_store_dwordx4 v[70:71], v[66:69], off nt
	s_nop 1
	v_or_b32_e32 v66, s4, v153
	v_or_b32_e32 v70, s29, v66
	ds_read_b128 v[66:69], v173
	v_ashrrev_i32_e32 v71, 31, v70
	v_lshlrev_b64 v[70:71], 10, v[70:71]
	v_lshl_add_u64 v[70:71], s[6:7], 0, v[70:71]
	v_lshl_add_u64 v[70:71], v[70:71], 0, v[134:135]
	s_waitcnt lgkmcnt(0)
	global_store_dwordx4 v[70:71], v[66:69], off nt
	s_nop 1
	v_or_b32_e32 v66, s4, v154
	v_or_b32_e32 v70, s29, v66
	ds_read_b128 v[66:69], v174
	v_ashrrev_i32_e32 v71, 31, v70
	v_lshlrev_b64 v[70:71], 10, v[70:71]
	v_lshl_add_u64 v[70:71], s[6:7], 0, v[70:71]
	v_lshl_add_u64 v[70:71], v[70:71], 0, v[134:135]
	s_waitcnt lgkmcnt(0)
	global_store_dwordx4 v[70:71], v[66:69], off nt
	s_nop 1
	v_or_b32_e32 v66, s4, v155
	v_or_b32_e32 v70, s29, v66
	ds_read_b128 v[66:69], v175
	v_ashrrev_i32_e32 v71, 31, v70
	v_lshlrev_b64 v[70:71], 10, v[70:71]
	v_lshl_add_u64 v[70:71], s[6:7], 0, v[70:71]
	v_lshl_add_u64 v[70:71], v[70:71], 0, v[134:135]
	s_waitcnt lgkmcnt(0)
	global_store_dwordx4 v[70:71], v[66:69], off nt
	s_waitcnt lgkmcnt(0)
	s_mov_b64 s[6:7], s[8:9]
	s_mov_b32 s29, s27
	s_cbranch_scc0 .LBB0_727

; __device__ __forceinline__ void unpack8(const v4u w, float (&y)[8]) { y[0] = bf_lo(w.x); y[1] = bf_hi(w.x); y[2] = bf_lo(w.y); y[3] = bf_hi(w.y); y[4] = bf_lo(w.z); y[5] = bf_hi(w.z); y[6] = bf_lo(w.w); y[7] = bf_hi(w.w); }
; __device__ __forceinline__ void combine_phase(bf16* x, const unsigned char* Y  , const int* SEL, const float* g, bf16* XN, float* fout, int gw, int NGW, int lane) {
;     ...
;     for (int row0 = R * gw; row0 < NTOK; row0 += R * NGW) {
;         const int b = row0 >> 13, s0 = row0 & (SEQ - 1);
;         bf16* xr = x + (size_t)row0 * DM + 8 * lane;
;         v4u w0[R], w1[R]; int sel[R];
;         const int* selp = SEL + ((size_t)b * NE + (lane & 15)) * SEQ + s0;
; #pragma unroll
;         for (int r = 0; r < R; ++r) { w0[r] = *(const v4u*)(xr + (size_t)r * DM); w1[r] = *(const v4u*)(xr + (size_t)r * DM + 512); sel[r] = selp[r]; }
;         float a[R][16]; unsigned mk[R];
; #pragma unroll
;         for (int r = 0; r < R; ++r) { float t[8]; unpack8(w0[r], t);
; #pragma unroll
;             for (int i = 0; i < 8; ++i) a[r][i] = t[i];
;             unpack8(w1[r], t);
; #pragma unroll
;             for (int i = 0; i < 8; ++i) a[r][8 + i] = t[i];
;             mk[r] = (unsigned)__ballot(sel[r] >= 0) & 0xffffu; }
;         constexpr int NI = 3;
;         { v2u y0[NI][R], y1[NI][R];
; #pragma unroll
;           for (int it = 0; it < NI; ++it)
; #pragma unroll
;             for (int r = 0; r < R; ++r) {
;                 const bool h = mk[r] != 0u; const int e = h ? __builtin_ctz(mk[r]) : 0; const int sl = __builtin_amdgcn_readlane(sel[r], e); mk[r] &= mk[r] - 1u;
;                 y0[it][r] = (v2u){0u, 0u}; y1[it][r] = y0[it][r];
;                 if (h) { const unsigned char* yr = Y + (((size_t)e * NB + b) * CAP + sl) * DM + 8 * lane; y0[it][r] = *(const v2u*)yr; y1[it][r] = *(const v2u*)(yr + 512); }
;             }
.LBB0_943:
	s_ashr_i32 s2, s6, 13
	s_ashr_i32 s3, s2, 31
	s_and_b32 s8, s6, 0x1ffc
	s_lshl_b64 s[14:15], s[2:3], 19
	v_lshl_add_u64 v[2:3], v[42:43], 0, s[14:15]
	s_lshl_b32 s8, s8, 2
	v_lshl_add_u64 v[2:3], v[2:3], 0, s[8:9]
	s_ashr_i32 s7, s6, 31
	global_load_dwordx4 v[2:5], v[2:3], off
	s_lshl_b64 s[12:13], s[6:7], 11
	v_lshl_add_u64 v[48:49], v[40:41], 0, s[12:13]
	v_add_co_u32_e32 v18, vcc, s22, v48
	global_load_dwordx4 v[34:37], v[48:49], off
	global_load_dwordx4 v[30:33], v[48:49], off offset:1024
	global_load_dwordx4 v[26:29], v[48:49], off offset:2048
	global_load_dwordx4 v[22:25], v[48:49], off offset:3072
	v_addc_co_u32_e32 v19, vcc, 0, v49, vcc
	global_load_dwordx4 v[14:17], v[18:19], off offset:1024
	global_load_dwordx4 v[10:13], v[18:19], off offset:2048
	global_load_dwordx4 v[6:9], v[18:19], off offset:3072
	s_nop 0
	global_load_dwordx4 v[18:21], v[18:19], off
	v_mov_b32_e32 v52, 0
	v_mov_b32_e32 v53, 0
	v_mov_b32_e32 v50, 0
	v_mov_b32_e32 v51, 0
	s_waitcnt vmcnt(0)
	v_cmp_lt_i32_e64 s[18:19], -1, v2
	v_cmp_lt_i32_e64 s[16:17], -1, v3
	s_and_b32 s17, s18, 0xffff
	s_cmp_eq_u32 s17, 0
	s_cselect_b64 s[20:21], -1, 0
	v_cmp_lt_i32_e64 s[12:13], -1, v5
	s_ff1_i32_b32 s8, s17
	s_and_b64 vcc, exec, s[20:21]
	s_cselect_b32 s13, 0, s8
	v_cmp_lt_i32_e64 s[14:15], -1, v4
	v_readlane_b32 s20, v2, s13
	s_cbranch_vccnz .LBB0_945
	s_lshl_b32 s8, s8, 2
	s_add_u32 s24, s8, s2
	s_addc_u32 s25, 0, s3
	s_ashr_i32 s21, s20, 31
	s_lshl_b64 s[24:25], s[24:25], 20
	s_lshl_b64 s[20:21], s[20:21], 10
	s_add_u32 s8, s94, s24
	s_addc_u32 s13, s95, s25
	s_add_u32 s20, s8, s20
	s_addc_u32 s21, s13, s21
	v_lshl_add_u64 v[50:51], s[20:21], 0, v[38:39]
	global_load_dwordx2 v[52:53], v[50:51], off nt
	s_nop 0
	global_load_dwordx2 v[50:51], v[50:51], off offset:512 nt
.LBB0_945:
	s_and_b32 s15, s16, 0xffff
	s_cmp_eq_u32 s15, 0
	s_cselect_b64 s[20:21], -1, 0
	s_ff1_i32_b32 s8, s15
	s_and_b64 vcc, s[20:21], exec
	s_cselect_b32 s13, 0, s8
	v_readlane_b32 s20, v3, s13
	v_mov_b32_e32 v54, 0
	v_mov_b32_e32 v58, 0
	v_mov_b32_e32 v59, 0
	v_mov_b32_e32 v56, 0
	v_mov_b32_e32 v57, 0
	s_cbranch_vccnz .LBB0_947
	s_lshl_b32 s8, s8, 2
	s_add_u32 s24, s8, s2
	s_addc_u32 s25, 0, s3
	s_ashr_i32 s21, s20, 31
	s_lshl_b64 s[24:25], s[24:25], 20
	s_lshl_b64 s[20:21], s[20:21], 10
	s_add_u32 s8, s94, s24
	s_addc_u32 s13, s95, s25
	s_add_u32 s20, s8, s20
	s_addc_u32 s21, s13, s21
	v_lshl_add_u64 v[56:57], s[20:21], 0, v[38:39]
	global_load_dwordx2 v[58:59], v[56:57], off nt
	s_nop 0
	global_load_dwordx2 v[56:57], v[56:57], off offset:512 nt
.LBB0_947:
	s_and_b32 s13, s14, 0xffff
	s_cmp_eq_u32 s13, 0
	s_cselect_b64 s[20:21], -1, 0
	s_ff1_i32_b32 s8, s13
	s_and_b64 vcc, s[20:21], exec
	s_cselect_b32 s19, 0, s8
	v_readlane_b32 s20, v4, s19
	v_mov_b32_e32 v55, 0
	v_mov_b32_e32 v60, 0
	v_mov_b32_e32 v61, 0
	s_cbranch_vccnz .LBB0_949
	s_lshl_b32 s8, s8, 2
	s_add_u32 s24, s8, s2
	s_addc_u32 s25, 0, s3
	s_ashr_i32 s21, s20, 31
	s_lshl_b64 s[24:25], s[24:25], 20
	s_lshl_b64 s[20:21], s[20:21], 10
	s_add_u32 s8, s94, s24
	s_addc_u32 s19, s95, s25
	s_add_u32 s20, s8, s20
	s_addc_u32 s21, s19, s21
	v_lshl_add_u64 v[60:61], s[20:21], 0, v[38:39]
	global_load_dwordx2 v[54:55], v[60:61], off nt
	s_nop 0
	global_load_dwordx2 v[60:61], v[60:61], off offset:512 nt
.LBB0_949:
	s_and_b32 s8, s12, 0xffff
	s_cmp_eq_u32 s8, 0
	s_cselect_b64 s[20:21], -1, 0
	s_ff1_i32_b32 s19, s8
	s_and_b64 vcc, s[20:21], exec
	s_cselect_b32 s20, 0, s19
	v_readlane_b32 s20, v5, s20
	v_mov_b32_e32 v62, 0
	v_mov_b32_e32 v66, 0
	v_mov_b32_e32 v67, 0
	v_mov_b32_e32 v64, 0
	v_mov_b32_e32 v65, 0
	s_cbranch_vccnz .LBB0_951
	s_lshl_b32 s19, s19, 2
	s_add_u32 s24, s19, s2
	s_addc_u32 s25, 0, s3
	s_ashr_i32 s21, s20, 31
	s_lshl_b64 s[24:25], s[24:25], 20
	s_lshl_b64 s[20:21], s[20:21], 10
	s_add_u32 s19, s94, s24
	s_addc_u32 s24, s95, s25
	s_add_u32 s20, s19, s20
	s_addc_u32 s21, s24, s21
	v_lshl_add_u64 v[64:65], s[20:21], 0, v[38:39]
	global_load_dwordx2 v[66:67], v[64:65], off nt
	s_nop 0
	global_load_dwordx2 v[64:65], v[64:65], off offset:512 nt
.LBB0_951:
	s_add_i32 s18, s18, -1
	s_and_b32 s20, s18, s17
	s_cmp_eq_u32 s20, 0
	s_cselect_b64 s[18:19], -1, 0
	s_ff1_i32_b32 s17, s20
	s_and_b64 vcc, s[18:19], exec
	s_cselect_b32 s18, 0, s17
	v_readlane_b32 s18, v2, s18
	v_mov_b32_e32 v63, 0
	v_mov_b32_e32 v68, 0
	v_mov_b32_e32 v69, 0
	s_cbranch_vccnz .LBB0_953
	s_lshl_b32 s17, s17, 2
	s_add_u32 s24, s17, s2
	s_addc_u32 s25, 0, s3
	s_ashr_i32 s19, s18, 31
	s_lshl_b64 s[24:25], s[24:25], 20
	s_lshl_b64 s[18:19], s[18:19], 10
	s_add_u32 s17, s94, s24
	s_addc_u32 s21, s95, s25
	s_add_u32 s18, s17, s18
	s_addc_u32 s19, s21, s19
	v_lshl_add_u64 v[68:69], s[18:19], 0, v[38:39]
	global_load_dwordx2 v[62:63], v[68:69], off nt
	s_nop 0
	global_load_dwordx2 v[68:69], v[68:69], off offset:512 nt
; __device__ __forceinline__ void combine_phase(bf16* x, const unsigned char* Y  , const int* SEL, const float* g, bf16* XN, float* fout, int gw, int NGW, int lane) {
;     ...
;         { v2u y0[NI][R], y1[NI][R];
; #pragma unroll
;           for (int it = 0; it < NI; ++it)
; #pragma unroll
;             for (int r = 0; r < R; ++r) {
;                 const bool h = mk[r] != 0u; const int e = h ? __builtin_ctz(mk[r]) : 0; const int sl = __builtin_amdgcn_readlane(sel[r], e); mk[r] &= mk[r] - 1u;
;                 y0[it][r] = (v2u){0u, 0u}; y1[it][r] = y0[it][r];
;                 if (h) { const unsigned char* yr = Y + (((size_t)e * NB + b) * CAP + sl) * DM + 8 * lane; y0[it][r] = *(const v2u*)yr; y1[it][r] = *(const v2u*)(yr + 512); }
;             }
.LBB0_953:
	s_add_i32 s16, s16, -1
	s_and_b32 s18, s16, s15
	s_cmp_eq_u32 s18, 0
	s_cselect_b64 s[16:17], -1, 0
	s_ff1_i32_b32 s15, s18
	s_and_b64 vcc, s[16:17], exec
	s_cselect_b32 s16, 0, s15
	v_readlane_b32 s16, v3, s16
	v_mov_b32_e32 v70, 0
	v_mov_b32_e32 v74, 0
	v_mov_b32_e32 v75, 0
	v_mov_b32_e32 v72, 0
	v_mov_b32_e32 v73, 0
	s_cbranch_vccnz .LBB0_955
	s_lshl_b32 s15, s15, 2
	s_add_u32 s24, s15, s2
	s_addc_u32 s25, 0, s3
	s_ashr_i32 s17, s16, 31
	s_lshl_b64 s[24:25], s[24:25], 20
	s_lshl_b64 s[16:17], s[16:17], 10
	s_add_u32 s15, s94, s24
	s_addc_u32 s19, s95, s25
	s_add_u32 s16, s15, s16
	s_addc_u32 s17, s19, s17
	v_lshl_add_u64 v[72:73], s[16:17], 0, v[38:39]
	global_load_dwordx2 v[74:75], v[72:73], off nt
	s_nop 0
	global_load_dwordx2 v[72:73], v[72:73], off offset:512 nt
.LBB0_955:
	s_add_i32 s14, s14, -1
	s_and_b32 s17, s14, s13
	s_cmp_eq_u32 s17, 0
	s_cselect_b64 s[14:15], -1, 0
	s_ff1_i32_b32 s13, s17
	s_and_b64 vcc, s[14:15], exec
	s_cselect_b32 s14, 0, s13
	v_readlane_b32 s14, v4, s14
	v_mov_b32_e32 v71, 0
	v_mov_b32_e32 v76, 0
	v_mov_b32_e32 v77, 0
	s_cbranch_vccnz .LBB0_957
	s_lshl_b32 s13, s13, 2
	s_add_u32 s24, s13, s2
	s_addc_u32 s25, 0, s3
	s_ashr_i32 s15, s14, 31
	s_lshl_b64 s[24:25], s[24:25], 20
	s_lshl_b64 s[14:15], s[14:15], 10
	s_add_u32 s13, s94, s24
	s_addc_u32 s16, s95, s25
	s_add_u32 s14, s13, s14
	s_addc_u32 s15, s16, s15
	v_lshl_add_u64 v[76:77], s[14:15], 0, v[38:39]
	global_load_dwordx2 v[70:71], v[76:77], off nt
	s_nop 0
	global_load_dwordx2 v[76:77], v[76:77], off offset:512 nt
.LBB0_957:
	s_add_i32 s12, s12, -1
	s_and_b32 s8, s12, s8
	s_cmp_eq_u32 s8, 0
	s_cselect_b64 s[14:15], -1, 0
	s_ff1_i32_b32 s13, s8
	s_and_b64 vcc, s[14:15], exec
	s_cselect_b32 s12, 0, s13
	v_readlane_b32 s12, v5, s12
	v_mov_b32_e32 v78, 0
	v_mov_b32_e32 v82, 0
	v_mov_b32_e32 v83, 0
	v_mov_b32_e32 v80, 0
	v_mov_b32_e32 v81, 0
	s_cbranch_vccnz .LBB0_959
	s_lshl_b32 s13, s13, 2
	s_add_u32 s14, s13, s2
	s_addc_u32 s15, 0, s3
	s_ashr_i32 s13, s12, 31
	s_lshl_b64 s[14:15], s[14:15], 20
	s_lshl_b64 s[12:13], s[12:13], 10
	s_add_u32 s14, s94, s14
	s_addc_u32 s15, s95, s15
	s_add_u32 s12, s14, s12
	s_addc_u32 s13, s15, s13
	v_lshl_add_u64 v[80:81], s[12:13], 0, v[38:39]
	global_load_dwordx2 v[82:83], v[80:81], off nt
	s_nop 0
	global_load_dwordx2 v[80:81], v[80:81], off offset:512 nt
.LBB0_959:
	s_add_i32 s12, s20, -1
	s_and_b32 s16, s12, s20
	s_cmp_eq_u32 s16, 0
	s_cselect_b64 s[14:15], -1, 0
	s_ff1_i32_b32 s13, s16
	s_and_b64 vcc, s[14:15], exec
	s_cselect_b32 s12, 0, s13
	v_readlane_b32 s12, v2, s12
	v_mov_b32_e32 v79, 0
	v_mov_b32_e32 v86, 0
	v_mov_b32_e32 v87, 0
	s_cbranch_vccnz .LBB0_961
	s_lshl_b32 s13, s13, 2
	s_add_u32 s14, s13, s2
	s_addc_u32 s15, 0, s3
	s_ashr_i32 s13, s12, 31
	s_lshl_b64 s[14:15], s[14:15], 20
	s_lshl_b64 s[12:13], s[12:13], 10
	s_add_u32 s14, s94, s14
	s_addc_u32 s15, s95, s15
	s_add_u32 s12, s14, s12
	s_addc_u32 s13, s15, s13
	v_lshl_add_u64 v[84:85], s[12:13], 0, v[38:39]
	global_load_dwordx2 v[78:79], v[84:85], off nt
	global_load_dwordx2 v[86:87], v[84:85], off offset:512 nt
.LBB0_961:
	s_add_i32 s12, s18, -1
	s_and_b32 s15, s12, s18
	s_cmp_eq_u32 s15, 0
	s_cselect_b64 s[18:19], -1, 0
	s_ff1_i32_b32 s13, s15
	s_and_b64 vcc, s[18:19], exec
	s_cselect_b32 s12, 0, s13
	v_readlane_b32 s12, v3, s12
	v_mov_b32_e32 v84, 0
	v_mov_b32_e32 v90, 0
	v_mov_b32_e32 v91, 0
	v_mov_b32_e32 v88, 0
	v_mov_b32_e32 v89, 0
	s_cbranch_vccnz .LBB0_963
	s_lshl_b32 s13, s13, 2
	s_add_u32 s18, s13, s2
	s_addc_u32 s19, 0, s3
	s_ashr_i32 s13, s12, 31
	s_lshl_b64 s[18:19], s[18:19], 20
	s_lshl_b64 s[12:13], s[12:13], 10
	s_add_u32 s14, s94, s18
	s_addc_u32 s18, s95, s19
	s_add_u32 s12, s14, s12
	s_addc_u32 s13, s18, s13
	v_lshl_add_u64 v[88:89], s[12:13], 0, v[38:39]
	global_load_dwordx2 v[90:91], v[88:89], off nt
	s_nop 0
	global_load_dwordx2 v[88:89], v[88:89], off offset:512 nt
.LBB0_963:
	s_add_i32 s12, s17, -1
	s_and_b32 s14, s12, s17
	s_cmp_eq_u32 s14, 0
	s_cselect_b64 s[18:19], -1, 0
	s_ff1_i32_b32 s13, s14
	s_and_b64 vcc, s[18:19], exec
	s_cselect_b32 s12, 0, s13
	v_readlane_b32 s12, v4, s12
	v_mov_b32_e32 v85, 0
	v_mov_b32_e32 v92, 0
	v_mov_b32_e32 v93, 0
	s_cbranch_vccnz .LBB0_965
	s_lshl_b32 s13, s13, 2
	s_add_u32 s18, s13, s2
	s_addc_u32 s19, 0, s3
	s_ashr_i32 s13, s12, 31
	s_lshl_b64 s[18:19], s[18:19], 20
	s_lshl_b64 s[12:13], s[12:13], 10
	s_add_u32 s17, s94, s18
	s_addc_u32 s18, s95, s19
	s_add_u32 s12, s17, s12
	s_addc_u32 s13, s18, s13
	v_lshl_add_u64 v[92:93], s[12:13], 0, v[38:39]
	global_load_dwordx2 v[84:85], v[92:93], off nt
	s_nop 0
	global_load_dwordx2 v[92:93], v[92:93], off offset:512 nt
.LBB0_965:
	s_add_i32 s12, s8, -1
	s_and_b32 s8, s12, s8
	s_cmp_eq_u32 s8, 0
	s_cselect_b64 s[18:19], -1, 0
	s_ff1_i32_b32 s13, s8
	s_and_b64 vcc, s[18:19], exec
	s_cselect_b32 s12, 0, s13
	v_readlane_b32 s12, v5, s12
	v_mov_b32_e32 v96, 0
	v_mov_b32_e32 v97, 0
	v_mov_b32_e32 v94, 0
	v_mov_b32_e32 v95, 0
	s_cbranch_vccnz .LBB0_967
	s_lshl_b32 s13, s13, 2
	s_add_u32 s18, s13, s2
	s_addc_u32 s19, 0, s3
	s_ashr_i32 s13, s12, 31
	s_lshl_b64 s[18:19], s[18:19], 20
	s_lshl_b64 s[12:13], s[12:13], 10
	s_add_u32 s17, s94, s18
	s_addc_u32 s18, s95, s19
	s_add_u32 s12, s17, s12
	s_addc_u32 s13, s18, s13
	v_lshl_add_u64 v[94:95], s[12:13], 0, v[38:39]
	global_load_dwordx2 v[96:97], v[94:95], off nt
	s_nop 0
	global_load_dwordx2 v[94:95], v[94:95], off offset:512 nt

; __device__ __forceinline__ void combine_phase(bf16* x, const unsigned char* Y  , const int* SEL, const float* g, bf16* XN, float* fout, int gw, int NGW, int lane) {
;     ...
;         while (mk[0] | mk[1] | mk[2] | mk[3]) {
;             v2u y0[R], y1[R];
; #pragma unroll
;             for (int r = 0; r < R; ++r) {
;                 const bool h = mk[r] != 0u; const int e = h ? __builtin_ctz(mk[r]) : 0; const int sl = __builtin_amdgcn_readlane(sel[r], e); mk[r] &= mk[r] - 1u;
;                 y0[r] = (v2u){0u, 0u}; y1[r] = y0[r];
;                 if (h) { const unsigned char* yr = Y + (((size_t)e * NB + b) * CAP + sl) * DM + 8 * lane; y0[r] = *(const v2u*)yr; y1[r] = *(const v2u*)(yr + 512); }
;             }
.LBB0_969:
	v_sub_co_u32_e64 v82, s[18:19], s16, 1
	s_ff1_i32_b32 s13, s16
	s_and_b64 vcc, s[18:19], exec
	s_cselect_b32 s12, 0, s13
	v_readfirstlane_b32 s17, v82
	v_readlane_b32 s12, v2, s12
	v_mov_b32_e32 v82, 0
	v_mov_b32_e32 v86, 0
	v_mov_b32_e32 v87, 0
	v_mov_b32_e32 v84, 0
	v_mov_b32_e32 v85, 0
	s_cbranch_vccnz .LBB0_971
	s_lshl_b32 s13, s13, 2
	s_add_u32 s18, s13, s2
	s_addc_u32 s19, 0, s3
	s_ashr_i32 s13, s12, 31
	s_lshl_b64 s[18:19], s[18:19], 20
	s_lshl_b64 s[12:13], s[12:13], 10
	s_add_u32 s18, s94, s18
	s_addc_u32 s19, s95, s19
	s_add_u32 s12, s18, s12
	s_addc_u32 s13, s19, s13
	v_lshl_add_u64 v[84:85], s[12:13], 0, v[38:39]
	global_load_dwordx2 v[86:87], v[84:85], off nt
	s_nop 0
	global_load_dwordx2 v[84:85], v[84:85], off offset:512 nt
.LBB0_971:
	v_sub_co_u32_e64 v83, s[20:21], s15, 1
	s_ff1_i32_b32 s13, s15
	s_and_b64 vcc, s[20:21], exec
	s_cselect_b32 s12, 0, s13
	v_readfirstlane_b32 s18, v83
	v_readlane_b32 s12, v3, s12
	v_mov_b32_e32 v83, 0
	v_mov_b32_e32 v88, 0
	v_mov_b32_e32 v89, 0
	s_cbranch_vccnz .LBB0_973
	s_lshl_b32 s13, s13, 2
	s_add_u32 s20, s13, s2
	s_addc_u32 s21, 0, s3
	s_ashr_i32 s13, s12, 31
	s_lshl_b64 s[20:21], s[20:21], 20
	s_lshl_b64 s[12:13], s[12:13], 10
	s_add_u32 s19, s94, s20
	s_addc_u32 s20, s95, s21
	s_add_u32 s12, s19, s12
	s_addc_u32 s13, s20, s13
	v_lshl_add_u64 v[88:89], s[12:13], 0, v[38:39]
	global_load_dwordx2 v[82:83], v[88:89], off nt
	s_nop 0
	global_load_dwordx2 v[88:89], v[88:89], off offset:512 nt
.LBB0_973:
	v_sub_co_u32_e64 v90, s[20:21], s14, 1
	s_ff1_i32_b32 s13, s14
	s_and_b64 vcc, s[20:21], exec
	s_cselect_b32 s12, 0, s13
	v_readfirstlane_b32 s19, v90
	v_readlane_b32 s12, v4, s12
	v_mov_b32_e32 v90, 0
	v_mov_b32_e32 v94, 0
	v_mov_b32_e32 v95, 0
	v_mov_b32_e32 v92, 0
	v_mov_b32_e32 v93, 0
	s_cbranch_vccnz .LBB0_975
	s_lshl_b32 s13, s13, 2
	s_add_u32 s20, s13, s2
	s_addc_u32 s21, 0, s3
	s_ashr_i32 s13, s12, 31
	s_lshl_b64 s[20:21], s[20:21], 20
	s_lshl_b64 s[12:13], s[12:13], 10
	s_add_u32 s20, s94, s20
	s_addc_u32 s21, s95, s21
	s_add_u32 s12, s20, s12
	s_addc_u32 s13, s21, s13
	v_lshl_add_u64 v[92:93], s[12:13], 0, v[38:39]
	global_load_dwordx2 v[94:95], v[92:93], off nt
	s_nop 0
	global_load_dwordx2 v[92:93], v[92:93], off offset:512 nt
.LBB0_975:
	v_sub_co_u32_e64 v91, s[24:25], s8, 1
	s_ff1_i32_b32 s13, s8
	s_and_b64 vcc, s[24:25], exec
	s_cselect_b32 s12, 0, s13
	v_readfirstlane_b32 s20, v91
	v_readlane_b32 s12, v5, s12
	v_mov_b32_e32 v91, 0
	v_mov_b32_e32 v96, 0
	v_mov_b32_e32 v97, 0
	s_cbranch_vccnz .LBB0_968
	s_lshl_b32 s13, s13, 2
	s_add_u32 s24, s13, s2
	s_addc_u32 s25, 0, s3
	s_ashr_i32 s13, s12, 31
	s_lshl_b64 s[24:25], s[24:25], 20
	s_lshl_b64 s[12:13], s[12:13], 10
	s_add_u32 s21, s94, s24
	s_addc_u32 s24, s95, s25
	s_add_u32 s12, s21, s12
	s_addc_u32 s13, s24, s13
	v_lshl_add_u64 v[96:97], s[12:13], 0, v[38:39]
	global_load_dwordx2 v[90:91], v[96:97], off nt
	s_nop 0
	global_load_dwordx2 v[96:97], v[96:97], off offset:512 nt
	s_branch .LBB0_968

; __device__ __forceinline__ void topk_phase(const float* AFF, int* IDX, float* GATE, int* SEL, LAS unsigned* sc, int G, int blk, int tid, int lane, int wave) {
;     ...
;         v4i* so = (v4i*)(SEL + ((size_t)b * NE + e) * SEQ) + 4 * tid;
; #pragma unroll
;         for (int j = 0; j < 4; ++j) so[j] = (v4i){sl[4 * j], sl[4 * j + 1], sl[4 * j + 2], sl[4 * j + 3]};
;         __syncthreads();
.LBB0_1324:
	s_or_b64 exec, exec, s[20:21]
	s_ashr_i32 s2, s88, 2
	s_lshl_b32 s3, s88, 4
	s_and_b32 s3, s3, 48
	s_ashr_i32 s20, s2, 31
	s_add_u32 s2, s3, s2
	s_addc_u32 s3, 0, s20
	s_lshl_b64 s[2:3], s[2:3], 15
	v_lshl_add_u64 v[2:3], v[24:25], 0, s[2:3]
	v_readlane_b32 s2, v254, 9
	s_add_i32 s88, s88, s2
	s_cmp_lt_i32 s88, 64
	global_store_dwordx4 v[2:3], v[18:21], off nt
	global_store_dwordx4 v[2:3], v[14:17], off offset:16 nt
	global_store_dwordx4 v[2:3], v[10:13], off offset:32 nt
	global_store_dwordx4 v[2:3], v[6:9], off offset:48 nt
	s_barrier
	s_cbranch_scc0 .LBB0_1444

; __device__ __forceinline__ unsigned pk4_fp8(float a, float b, float c, float d) { unsigned w = 0u; w = __builtin_amdgcn_cvt_pk_fp8_f32(a, b, w, false); w = __builtin_amdgcn_cvt_pk_fp8_f32(c, d, w, true); return w; }
; #define LAS __attribute__((address_space(3)))
; #define LDS_WAIT() asm volatile("s_waitcnt lgkmcnt(0)" ::: "memory")
; __device__ __forceinline__ void cvt_pack8(const f32x4 (&v)[16], const CvtItem& c, LAS unsigned char* blk, int s4, int lane) {
;     const float w = c.wscale; const int cb = lane & 15, j = 4 * s4 + (lane >> 4);
; #pragma unroll
;     for (int jn = 0; jn < 4; ++jn) {
;         v4u o; o.x = pg8::pk4_fp8(v[0][jn] * w, v[1][jn] * w, v[2][jn] * w, v[3][jn] * w); o.y = pg8::pk4_fp8(v[4][jn] * w, v[5][jn] * w, v[6][jn] * w, v[7][jn] * w);
;         o.z = pg8::pk4_fp8(v[8][jn] * w, v[9][jn] * w, v[10][jn] * w, v[11][jn] * w); o.w = pg8::pk4_fp8(v[12][jn] * w, v[13][jn] * w, v[14][jn] * w, v[15][jn] * w);
;         *(LAS v4u*)(blk + (4 * cb + jn) * 256 + ((j ^ cb) * 16)) = o; }
; }
; __device__ __forceinline__ void cvt_flush8(const CvtItem& c, const LAS unsigned char* blk, int lane) {
;     LDS_WAIT();
; #pragma unroll
;     for (int t = 0; t < 16; ++t) { const int idx = 64 * t + lane, n = idx >> 4, pc = idx & 15, nn = c.nb * 64 + n;
;         const size_t row = (c.which < 2) ? (size_t)((nn >> 7) * 256 + (nn & 127) + c.which * 128) : (size_t)nn;
;         *(v4u*)(c.dst + row * c.K + 16 * pc) = *(const LAS v4u*)(blk + n * 256 + ((pc ^ ((n >> 2) & 15)) * 16)); }
;     LDS_WAIT();
.LBB0_1448:
	s_waitcnt vmcnt(7)
	v_mul_f32_e32 v66, v179, v66
	s_waitcnt vmcnt(6)
	v_mul_f32_e32 v70, v179, v70
	v_mov_b32_e32 v180, 0
	v_cvt_pk_fp8_f32 v180, v66, v70
	v_mul_f32_e32 v66, v179, v78
	v_mul_f32_e32 v70, v179, v90
	v_mov_b32_e32 v181, 0
	v_cvt_pk_fp8_f32 v181, v66, v70
	s_waitcnt vmcnt(5)
	v_mul_f32_e32 v66, v179, v82
	s_waitcnt vmcnt(4)
	v_mul_f32_e32 v70, v179, v98
	v_mov_b32_e32 v182, 0
	v_cvt_pk_fp8_f32 v182, v66, v70
	s_waitcnt vmcnt(3)
	v_mul_f32_e32 v66, v179, v106
	s_waitcnt vmcnt(2)
	v_mul_f32_e32 v70, v179, v118
	v_mov_b32_e32 v183, 0
	v_mul_f32_e32 v74, v179, v74
	v_mul_f32_e32 v86, v179, v86
	v_cvt_pk_fp8_f32 v183, v66, v70
	v_cvt_pk_fp8_f32 v180, v74, v86 op_sel:[0,0,1]
	v_mul_f32_e32 v74, v179, v94
	v_mul_f32_e32 v78, v179, v110
	v_cvt_pk_fp8_f32 v181, v74, v78 op_sel:[0,0,1]
	v_mul_f32_e32 v74, v179, v102
	v_mul_f32_e32 v78, v179, v114
	v_cvt_pk_fp8_f32 v182, v74, v78 op_sel:[0,0,1]
	s_waitcnt vmcnt(1)
	v_mul_f32_e32 v74, v179, v122
	s_waitcnt vmcnt(0)
	v_mul_f32_e32 v78, v179, v126
	v_cvt_pk_fp8_f32 v183, v74, v78 op_sel:[0,0,1]
	v_mul_f32_e32 v66, v179, v67
	v_mul_f32_e32 v67, v179, v71
	v_mul_f32_e32 v70, v179, v75
	ds_write_b128 v161, v[180:183]
	v_mov_b32_e32 v180, 0
	v_cvt_pk_fp8_f32 v180, v66, v67
	v_mul_f32_e32 v66, v179, v79
	v_mul_f32_e32 v67, v179, v91
	v_mov_b32_e32 v181, 0
	v_cvt_pk_fp8_f32 v181, v66, v67
	v_mul_f32_e32 v66, v179, v83
	v_mul_f32_e32 v67, v179, v99
	v_mov_b32_e32 v182, 0
	v_cvt_pk_fp8_f32 v182, v66, v67
	v_mul_f32_e32 v66, v179, v107
	v_mul_f32_e32 v67, v179, v119
	v_mov_b32_e32 v183, 0
	v_mul_f32_e32 v71, v179, v87
	v_cvt_pk_fp8_f32 v183, v66, v67
	v_cvt_pk_fp8_f32 v180, v70, v71 op_sel:[0,0,1]
	v_mul_f32_e32 v70, v179, v95
	v_mul_f32_e32 v71, v179, v111
	v_cvt_pk_fp8_f32 v181, v70, v71 op_sel:[0,0,1]
	v_mul_f32_e32 v70, v179, v103
	v_mul_f32_e32 v71, v179, v115
	v_cvt_pk_fp8_f32 v182, v70, v71 op_sel:[0,0,1]
	v_mul_f32_e32 v70, v179, v123
	v_mul_f32_e32 v71, v179, v127
	v_cvt_pk_fp8_f32 v183, v70, v71 op_sel:[0,0,1]
	v_mul_f32_e32 v66, v179, v68
	v_mul_f32_e32 v67, v179, v72
	v_mul_f32_e32 v68, v179, v76
	ds_write_b128 v161, v[180:183] offset:256
	v_mov_b32_e32 v180, 0
	v_cvt_pk_fp8_f32 v180, v66, v67
	v_mul_f32_e32 v66, v179, v80
	v_mul_f32_e32 v67, v179, v92
	v_mov_b32_e32 v181, 0
	v_cvt_pk_fp8_f32 v181, v66, v67
	v_mul_f32_e32 v66, v179, v84
	v_mul_f32_e32 v67, v179, v100
	v_mov_b32_e32 v182, 0
	v_cvt_pk_fp8_f32 v182, v66, v67
	v_mul_f32_e32 v66, v179, v108
	v_mul_f32_e32 v67, v179, v120
	v_mov_b32_e32 v183, 0
	v_mul_f32_e32 v70, v179, v88
	v_cvt_pk_fp8_f32 v183, v66, v67
	v_cvt_pk_fp8_f32 v180, v68, v70 op_sel:[0,0,1]
	v_mul_f32_e32 v68, v179, v96
	v_mul_f32_e32 v70, v179, v112
	v_cvt_pk_fp8_f32 v181, v68, v70 op_sel:[0,0,1]
	v_mul_f32_e32 v68, v179, v104
	v_mul_f32_e32 v70, v179, v116
	v_cvt_pk_fp8_f32 v182, v68, v70 op_sel:[0,0,1]
	v_mul_f32_e32 v68, v179, v124
	v_mul_f32_e32 v70, v179, v128
	v_cvt_pk_fp8_f32 v183, v68, v70 op_sel:[0,0,1]
	v_mul_f32_e32 v67, v179, v69
	v_mul_f32_e32 v68, v179, v73
	v_mov_b32_e32 v66, 0
	v_cvt_pk_fp8_f32 v66, v67, v68
	v_mul_f32_e32 v69, v179, v77
	v_mul_f32_e32 v70, v179, v89
	v_mul_f32_e32 v68, v179, v81
	v_cvt_pk_fp8_f32 v66, v69, v70 op_sel:[0,0,1]
	v_mul_f32_e32 v69, v179, v93
	v_mov_b32_e32 v67, 0
	v_cvt_pk_fp8_f32 v67, v68, v69
	v_mul_f32_e32 v70, v179, v97
	v_mul_f32_e32 v71, v179, v113
	v_mul_f32_e32 v69, v179, v85
	v_cvt_pk_fp8_f32 v67, v70, v71 op_sel:[0,0,1]
	v_mul_f32_e32 v70, v179, v101
	v_mov_b32_e32 v68, 0
	v_cvt_pk_fp8_f32 v68, v69, v70
	v_mul_f32_e32 v71, v179, v105
	v_mul_f32_e32 v72, v179, v117
	v_mul_f32_e32 v70, v179, v109
	v_cvt_pk_fp8_f32 v68, v71, v72 op_sel:[0,0,1]
	v_mul_f32_e32 v71, v179, v121
	v_mov_b32_e32 v69, 0
	v_cvt_pk_fp8_f32 v69, v70, v71
	v_mul_f32_e32 v72, v179, v125
	v_mul_f32_e32 v73, v179, v129
	s_lshl_b32 s4, s57, 6
	v_cvt_pk_fp8_f32 v69, v72, v73 op_sel:[0,0,1]
	s_and_b32 s33, s57, 0x1fffffe
	ds_write_b128 v161, v[180:183] offset:512
	s_and_b32 s4, s4, 64
	ds_write_b128 v161, v[66:69] offset:768
	s_add_i32 s33, s33, s56
	s_waitcnt lgkmcnt(0)
	v_or_b32_e32 v66, s4, v142
	s_lshl_b32 s33, s33, 7
	v_or_b32_e32 v70, s33, v66
	ds_read_b128 v[66:69], v162
	v_ashrrev_i32_e32 v71, 31, v70
	v_lshlrev_b64 v[70:71], 10, v[70:71]
	v_lshl_add_u64 v[70:71], s[6:7], 0, v[70:71]
	v_lshl_add_u64 v[70:71], v[70:71], 0, v[134:135]
	s_waitcnt lgkmcnt(0)
	global_store_dwordx4 v[70:71], v[66:69], off nt
	s_add_i32 s25, s25, s26
	s_andn2_b64 vcc, exec, s[2:3]
	v_or_b32_e32 v66, s4, v143
	v_or_b32_e32 v70, s33, v66
	ds_read_b128 v[66:69], v163
	v_ashrrev_i32_e32 v71, 31, v70
	v_lshlrev_b64 v[70:71], 10, v[70:71]
	v_lshl_add_u64 v[70:71], s[6:7], 0, v[70:71]
	v_lshl_add_u64 v[70:71], v[70:71], 0, v[134:135]
	s_waitcnt lgkmcnt(0)
; #define LAS __attribute__((address_space(3)))
; #define LDS_WAIT() asm volatile("s_waitcnt lgkmcnt(0)" ::: "memory")
; __device__ __forceinline__ void cvt_flush8(const CvtItem& c, const LAS unsigned char* blk, int lane) {
;     LDS_WAIT();
; #pragma unroll
;     for (int t = 0; t < 16; ++t) { const int idx = 64 * t + lane, n = idx >> 4, pc = idx & 15, nn = c.nb * 64 + n;
;         const size_t row = (c.which < 2) ? (size_t)((nn >> 7) * 256 + (nn & 127) + c.which * 128) : (size_t)nn;
;         *(v4u*)(c.dst + row * c.K + 16 * pc) = *(const LAS v4u*)(blk + n * 256 + ((pc ^ ((n >> 2) & 15)) * 16)); }
;     LDS_WAIT();
	global_store_dwordx4 v[70:71], v[66:69], off nt
	s_mov_b32 s56, s53
	s_mov_b32 s57, s54
	v_or_b32_e32 v66, s4, v144
	v_or_b32_e32 v70, s33, v66
	ds_read_b128 v[66:69], v164
	v_ashrrev_i32_e32 v71, 31, v70
	v_lshlrev_b64 v[70:71], 10, v[70:71]
	v_lshl_add_u64 v[70:71], s[6:7], 0, v[70:71]
	v_lshl_add_u64 v[70:71], v[70:71], 0, v[134:135]
	s_waitcnt lgkmcnt(0)
	global_store_dwordx4 v[70:71], v[66:69], off nt
	v_mov_b32_e32 v179, v178
	s_nop 0
	v_or_b32_e32 v66, s4, v145
	v_or_b32_e32 v70, s33, v66
	ds_read_b128 v[66:69], v165
	v_ashrrev_i32_e32 v71, 31, v70
	v_lshlrev_b64 v[70:71], 10, v[70:71]
	v_lshl_add_u64 v[70:71], s[6:7], 0, v[70:71]
	v_lshl_add_u64 v[70:71], v[70:71], 0, v[134:135]
	s_waitcnt lgkmcnt(0)
	global_store_dwordx4 v[70:71], v[66:69], off nt
	s_nop 1
	v_or_b32_e32 v66, s4, v146
	v_or_b32_e32 v70, s33, v66
	ds_read_b128 v[66:69], v166
	v_ashrrev_i32_e32 v71, 31, v70
	v_lshlrev_b64 v[70:71], 10, v[70:71]
	v_lshl_add_u64 v[70:71], s[6:7], 0, v[70:71]
	v_lshl_add_u64 v[70:71], v[70:71], 0, v[134:135]
	s_waitcnt lgkmcnt(0)
	global_store_dwordx4 v[70:71], v[66:69], off nt
	s_nop 1
	v_or_b32_e32 v66, s4, v147
	v_or_b32_e32 v70, s33, v66
	ds_read_b128 v[66:69], v167
	v_ashrrev_i32_e32 v71, 31, v70
	v_lshlrev_b64 v[70:71], 10, v[70:71]
	v_lshl_add_u64 v[70:71], s[6:7], 0, v[70:71]
	v_lshl_add_u64 v[70:71], v[70:71], 0, v[134:135]
	s_waitcnt lgkmcnt(0)
	global_store_dwordx4 v[70:71], v[66:69], off nt
	s_nop 1
	v_or_b32_e32 v66, s4, v148
	v_or_b32_e32 v70, s33, v66
	ds_read_b128 v[66:69], v168
	v_ashrrev_i32_e32 v71, 31, v70
	v_lshlrev_b64 v[70:71], 10, v[70:71]
	v_lshl_add_u64 v[70:71], s[6:7], 0, v[70:71]
	v_lshl_add_u64 v[70:71], v[70:71], 0, v[134:135]
	s_waitcnt lgkmcnt(0)
	global_store_dwordx4 v[70:71], v[66:69], off nt
	s_nop 1
	v_or_b32_e32 v66, s4, v149
	v_or_b32_e32 v70, s33, v66
	ds_read_b128 v[66:69], v169
	v_ashrrev_i32_e32 v71, 31, v70
	v_lshlrev_b64 v[70:71], 10, v[70:71]
	v_lshl_add_u64 v[70:71], s[6:7], 0, v[70:71]
	v_lshl_add_u64 v[70:71], v[70:71], 0, v[134:135]
	s_waitcnt lgkmcnt(0)
	global_store_dwordx4 v[70:71], v[66:69], off nt
	s_nop 1
	v_or_b32_e32 v66, s4, v150
	v_or_b32_e32 v70, s33, v66
	ds_read_b128 v[66:69], v170
	v_ashrrev_i32_e32 v71, 31, v70
	v_lshlrev_b64 v[70:71], 10, v[70:71]
	v_lshl_add_u64 v[70:71], s[6:7], 0, v[70:71]
	v_lshl_add_u64 v[70:71], v[70:71], 0, v[134:135]
	s_waitcnt lgkmcnt(0)
	global_store_dwordx4 v[70:71], v[66:69], off nt
	s_nop 1
	v_or_b32_e32 v66, s4, v151
	v_or_b32_e32 v70, s33, v66
	ds_read_b128 v[66:69], v171
	v_ashrrev_i32_e32 v71, 31, v70
	v_lshlrev_b64 v[70:71], 10, v[70:71]
	v_lshl_add_u64 v[70:71], s[6:7], 0, v[70:71]
	v_lshl_add_u64 v[70:71], v[70:71], 0, v[134:135]
	s_waitcnt lgkmcnt(0)
	global_store_dwordx4 v[70:71], v[66:69], off nt
	s_nop 1
	v_or_b32_e32 v66, s4, v152
	v_or_b32_e32 v70, s33, v66
	ds_read_b128 v[66:69], v172
	v_ashrrev_i32_e32 v71, 31, v70
	v_lshlrev_b64 v[70:71], 10, v[70:71]
	v_lshl_add_u64 v[70:71], s[6:7], 0, v[70:71]
	v_lshl_add_u64 v[70:71], v[70:71], 0, v[134:135]
	s_waitcnt lgkmcnt(0)
	global_store_dwordx4 v[70:71], v[66:69], off nt
	s_nop 1
	v_or_b32_e32 v66, s4, v153
	v_or_b32_e32 v70, s33, v66
	ds_read_b128 v[66:69], v173
	v_ashrrev_i32_e32 v71, 31, v70
	v_lshlrev_b64 v[70:71], 10, v[70:71]
	v_lshl_add_u64 v[70:71], s[6:7], 0, v[70:71]
	v_lshl_add_u64 v[70:71], v[70:71], 0, v[134:135]
	s_waitcnt lgkmcnt(0)
	global_store_dwordx4 v[70:71], v[66:69], off nt
	s_nop 1
	v_or_b32_e32 v66, s4, v154
	v_or_b32_e32 v70, s33, v66
	ds_read_b128 v[66:69], v174
	v_ashrrev_i32_e32 v71, 31, v70
	v_lshlrev_b64 v[70:71], 10, v[70:71]
	v_lshl_add_u64 v[70:71], s[6:7], 0, v[70:71]
	v_lshl_add_u64 v[70:71], v[70:71], 0, v[134:135]
	s_waitcnt lgkmcnt(0)
	global_store_dwordx4 v[70:71], v[66:69], off nt
	s_nop 1
	v_or_b32_e32 v66, s4, v155
	v_or_b32_e32 v70, s33, v66
	ds_read_b128 v[66:69], v175
	v_ashrrev_i32_e32 v71, 31, v70
	v_lshlrev_b64 v[70:71], 10, v[70:71]
	v_lshl_add_u64 v[70:71], s[6:7], 0, v[70:71]
	v_lshl_add_u64 v[70:71], v[70:71], 0, v[134:135]
	s_waitcnt lgkmcnt(0)
	global_store_dwordx4 v[70:71], v[66:69], off nt
	s_nop 1
	v_or_b32_e32 v66, s4, v156
	v_or_b32_e32 v70, s33, v66
	ds_read_b128 v[66:69], v176
	v_ashrrev_i32_e32 v71, 31, v70
	v_lshlrev_b64 v[70:71], 10, v[70:71]
	v_lshl_add_u64 v[70:71], s[6:7], 0, v[70:71]
	v_lshl_add_u64 v[70:71], v[70:71], 0, v[134:135]
	s_waitcnt lgkmcnt(0)
	global_store_dwordx4 v[70:71], v[66:69], off nt
	s_nop 1
	v_or_b32_e32 v66, s4, v157
	v_or_b32_e32 v70, s33, v66
	ds_read_b128 v[66:69], v177
	v_ashrrev_i32_e32 v71, 31, v70
	v_lshlrev_b64 v[70:71], 10, v[70:71]
	v_lshl_add_u64 v[70:71], s[6:7], 0, v[70:71]
	v_lshl_add_u64 v[70:71], v[70:71], 0, v[134:135]
	s_waitcnt lgkmcnt(0)
	global_store_dwordx4 v[70:71], v[66:69], off nt
	s_waitcnt lgkmcnt(0)
	s_mov_b64 s[6:7], s[8:9]
	s_cbranch_vccz .LBB0_1451

; __device__ __forceinline__ unsigned pk4_fp8(float a, float b, float c, float d) { unsigned w = 0u; w = __builtin_amdgcn_cvt_pk_fp8_f32(a, b, w, false); w = __builtin_amdgcn_cvt_pk_fp8_f32(c, d, w, true); return w; }
; #define LAS __attribute__((address_space(3)))
; #define LDS_WAIT() asm volatile("s_waitcnt lgkmcnt(0)" ::: "memory")
; __device__ __forceinline__ void cvt_pack8(const f32x4 (&v)[16], const CvtItem& c, LAS unsigned char* blk, int s4, int lane) {
;     const float w = c.wscale; const int cb = lane & 15, j = 4 * s4 + (lane >> 4);
; #pragma unroll
;     for (int jn = 0; jn < 4; ++jn) {
;         v4u o; o.x = pg8::pk4_fp8(v[0][jn] * w, v[1][jn] * w, v[2][jn] * w, v[3][jn] * w); o.y = pg8::pk4_fp8(v[4][jn] * w, v[5][jn] * w, v[6][jn] * w, v[7][jn] * w);
;         o.z = pg8::pk4_fp8(v[8][jn] * w, v[9][jn] * w, v[10][jn] * w, v[11][jn] * w); o.w = pg8::pk4_fp8(v[12][jn] * w, v[13][jn] * w, v[14][jn] * w, v[15][jn] * w);
;         *(LAS v4u*)(blk + (4 * cb + jn) * 256 + ((j ^ cb) * 16)) = o; }
; }
; __device__ __forceinline__ void cvt_flush8(const CvtItem& c, const LAS unsigned char* blk, int lane) {
;     LDS_WAIT();
; #pragma unroll
;     for (int t = 0; t < 16; ++t) { const int idx = 64 * t + lane, n = idx >> 4, pc = idx & 15, nn = c.nb * 64 + n;
;         const size_t row = (c.which < 2) ? (size_t)((nn >> 7) * 256 + (nn & 127) + c.which * 128) : (size_t)nn;
;         *(v4u*)(c.dst + row * c.K + 16 * pc) = *(const LAS v4u*)(blk + n * 256 + ((pc ^ ((n >> 2) & 15)) * 16)); }
;     LDS_WAIT();
.LBB0_1455:
	s_waitcnt vmcnt(7)
	v_mul_f32_e32 v66, v177, v66
	s_waitcnt vmcnt(6)
	v_mul_f32_e32 v70, v177, v70
	v_mov_b32_e32 v178, 0
	v_cvt_pk_fp8_f32 v178, v66, v70
	v_mul_f32_e32 v66, v177, v78
	v_mul_f32_e32 v70, v177, v90
	v_mov_b32_e32 v179, 0
	v_cvt_pk_fp8_f32 v179, v66, v70
	s_waitcnt vmcnt(5)
	v_mul_f32_e32 v66, v177, v82
	s_waitcnt vmcnt(4)
	v_mul_f32_e32 v70, v177, v98
	v_mov_b32_e32 v180, 0
	v_cvt_pk_fp8_f32 v180, v66, v70
	s_waitcnt vmcnt(3)
	v_mul_f32_e32 v66, v177, v106
	s_waitcnt vmcnt(2)
	v_mul_f32_e32 v70, v177, v118
	v_mov_b32_e32 v181, 0
	v_mul_f32_e32 v74, v177, v74
	v_mul_f32_e32 v86, v177, v86
	v_cvt_pk_fp8_f32 v181, v66, v70
	v_cvt_pk_fp8_f32 v178, v74, v86 op_sel:[0,0,1]
	v_mul_f32_e32 v74, v177, v94
	v_mul_f32_e32 v78, v177, v110
	v_cvt_pk_fp8_f32 v179, v74, v78 op_sel:[0,0,1]
	v_mul_f32_e32 v74, v177, v102
	v_mul_f32_e32 v78, v177, v114
	v_cvt_pk_fp8_f32 v180, v74, v78 op_sel:[0,0,1]
	s_waitcnt vmcnt(1)
	v_mul_f32_e32 v74, v177, v122
	s_waitcnt vmcnt(0)
	v_mul_f32_e32 v78, v177, v126
	v_cvt_pk_fp8_f32 v181, v74, v78 op_sel:[0,0,1]
	v_mul_f32_e32 v66, v177, v67
	v_mul_f32_e32 v67, v177, v71
	v_mul_f32_e32 v70, v177, v75
	ds_write_b128 v159, v[178:181]
	v_mov_b32_e32 v178, 0
	v_cvt_pk_fp8_f32 v178, v66, v67
	v_mul_f32_e32 v66, v177, v79
	v_mul_f32_e32 v67, v177, v91
	v_mov_b32_e32 v179, 0
	v_cvt_pk_fp8_f32 v179, v66, v67
	v_mul_f32_e32 v66, v177, v83
	v_mul_f32_e32 v67, v177, v99
	v_mov_b32_e32 v180, 0
	v_cvt_pk_fp8_f32 v180, v66, v67
	v_mul_f32_e32 v66, v177, v107
	v_mul_f32_e32 v67, v177, v119
	v_mov_b32_e32 v181, 0
	v_mul_f32_e32 v71, v177, v87
	v_cvt_pk_fp8_f32 v181, v66, v67
	v_cvt_pk_fp8_f32 v178, v70, v71 op_sel:[0,0,1]
	v_mul_f32_e32 v70, v177, v95
	v_mul_f32_e32 v71, v177, v111
	v_cvt_pk_fp8_f32 v179, v70, v71 op_sel:[0,0,1]
	v_mul_f32_e32 v70, v177, v103
	v_mul_f32_e32 v71, v177, v115
	v_cvt_pk_fp8_f32 v180, v70, v71 op_sel:[0,0,1]
	v_mul_f32_e32 v70, v177, v123
	v_mul_f32_e32 v71, v177, v127
	v_cvt_pk_fp8_f32 v181, v70, v71 op_sel:[0,0,1]
	v_mul_f32_e32 v66, v177, v68
	v_mul_f32_e32 v67, v177, v72
	v_mul_f32_e32 v68, v177, v76
	ds_write_b128 v159, v[178:181] offset:256
	v_mov_b32_e32 v178, 0
	v_cvt_pk_fp8_f32 v178, v66, v67
	v_mul_f32_e32 v66, v177, v80
	v_mul_f32_e32 v67, v177, v92
	v_mov_b32_e32 v179, 0
	v_cvt_pk_fp8_f32 v179, v66, v67
	v_mul_f32_e32 v66, v177, v84
	v_mul_f32_e32 v67, v177, v100
	v_mov_b32_e32 v180, 0
	v_cvt_pk_fp8_f32 v180, v66, v67
	v_mul_f32_e32 v66, v177, v108
	v_mul_f32_e32 v67, v177, v120
	v_mov_b32_e32 v181, 0
	v_mul_f32_e32 v70, v177, v88
	v_cvt_pk_fp8_f32 v181, v66, v67
	v_cvt_pk_fp8_f32 v178, v68, v70 op_sel:[0,0,1]
	v_mul_f32_e32 v68, v177, v96
	v_mul_f32_e32 v70, v177, v112
	v_cvt_pk_fp8_f32 v179, v68, v70 op_sel:[0,0,1]
	v_mul_f32_e32 v68, v177, v104
	v_mul_f32_e32 v70, v177, v116
	v_cvt_pk_fp8_f32 v180, v68, v70 op_sel:[0,0,1]
	v_mul_f32_e32 v68, v177, v124
	v_mul_f32_e32 v70, v177, v128
	v_cvt_pk_fp8_f32 v181, v68, v70 op_sel:[0,0,1]
	v_mul_f32_e32 v67, v177, v69
	v_mul_f32_e32 v68, v177, v73
	v_mov_b32_e32 v66, 0
	v_cvt_pk_fp8_f32 v66, v67, v68
	v_mul_f32_e32 v69, v177, v77
	v_mul_f32_e32 v70, v177, v89
	v_mul_f32_e32 v68, v177, v81
	v_cvt_pk_fp8_f32 v66, v69, v70 op_sel:[0,0,1]
	v_mul_f32_e32 v69, v177, v93
	v_mov_b32_e32 v67, 0
	v_cvt_pk_fp8_f32 v67, v68, v69
	v_mul_f32_e32 v70, v177, v97
	v_mul_f32_e32 v71, v177, v113
	v_mul_f32_e32 v69, v177, v85
	v_cvt_pk_fp8_f32 v67, v70, v71 op_sel:[0,0,1]
	v_mul_f32_e32 v70, v177, v101
	v_mov_b32_e32 v68, 0
	v_cvt_pk_fp8_f32 v68, v69, v70
	v_mul_f32_e32 v71, v177, v105
	v_mul_f32_e32 v72, v177, v117
	v_mul_f32_e32 v70, v177, v109
	v_cvt_pk_fp8_f32 v68, v71, v72 op_sel:[0,0,1]
	v_mul_f32_e32 v71, v177, v121
	v_mov_b32_e32 v69, 0
	v_cvt_pk_fp8_f32 v69, v70, v71
	v_mul_f32_e32 v72, v177, v125
	v_mul_f32_e32 v73, v177, v129
	s_lshl_b32 s4, s57, 6
	v_cvt_pk_fp8_f32 v69, v72, v73 op_sel:[0,0,1]
	s_and_b32 s33, s57, 0x1fffffe
	ds_write_b128 v159, v[178:181] offset:512
	s_and_b32 s4, s4, 64
	ds_write_b128 v159, v[66:69] offset:768
	s_add_i32 s33, s33, s56
	s_waitcnt lgkmcnt(0)
	v_or_b32_e32 v66, s4, v138
	s_lshl_b32 s33, s33, 7
	v_or_b32_e32 v70, s33, v66
	ds_read_b128 v[66:69], v160
	v_ashrrev_i32_e32 v71, 31, v70
	v_lshlrev_b64 v[70:71], 10, v[70:71]
	v_lshl_add_u64 v[70:71], s[6:7], 0, v[70:71]
	v_lshl_add_u64 v[70:71], v[70:71], 0, v[134:135]
	s_waitcnt lgkmcnt(0)
	global_store_dwordx4 v[70:71], v[66:69], off nt
	s_add_i32 s2, s2, s3
	s_add_i32 s25, s25, s26
	v_or_b32_e32 v66, s4, v1
	v_or_b32_e32 v70, s33, v66
	ds_read_b128 v[66:69], v161
	v_ashrrev_i32_e32 v71, 31, v70
	v_lshlrev_b64 v[70:71], 10, v[70:71]
	v_lshl_add_u64 v[70:71], s[6:7], 0, v[70:71]
	v_lshl_add_u64 v[70:71], v[70:71], 0, v[134:135]
	s_waitcnt lgkmcnt(0)
; #define LAS __attribute__((address_space(3)))
; #define LDS_WAIT() asm volatile("s_waitcnt lgkmcnt(0)" ::: "memory")
; __device__ __forceinline__ void cvt_flush8(const CvtItem& c, const LAS unsigned char* blk, int lane) {
;     LDS_WAIT();
; #pragma unroll
;     for (int t = 0; t < 16; ++t) { const int idx = 64 * t + lane, n = idx >> 4, pc = idx & 15, nn = c.nb * 64 + n;
;         const size_t row = (c.which < 2) ? (size_t)((nn >> 7) * 256 + (nn & 127) + c.which * 128) : (size_t)nn;
;         *(v4u*)(c.dst + row * c.K + 16 * pc) = *(const LAS v4u*)(blk + n * 256 + ((pc ^ ((n >> 2) & 15)) * 16)); }
;     LDS_WAIT();
	global_store_dwordx4 v[70:71], v[66:69], off nt
	s_mov_b32 s56, s54
	s_mov_b32 s57, s55
	v_or_b32_e32 v66, s4, v142
	v_or_b32_e32 v70, s33, v66
	ds_read_b128 v[66:69], v162
	v_ashrrev_i32_e32 v71, 31, v70
	v_lshlrev_b64 v[70:71], 10, v[70:71]
	v_lshl_add_u64 v[70:71], s[6:7], 0, v[70:71]
	v_lshl_add_u64 v[70:71], v[70:71], 0, v[134:135]
	s_waitcnt lgkmcnt(0)
	global_store_dwordx4 v[70:71], v[66:69], off nt
	v_mov_b32_e32 v177, v176
	s_nop 0
	v_or_b32_e32 v66, s4, v143
	v_or_b32_e32 v70, s33, v66
	ds_read_b128 v[66:69], v163
	v_ashrrev_i32_e32 v71, 31, v70
	v_lshlrev_b64 v[70:71], 10, v[70:71]
	v_lshl_add_u64 v[70:71], s[6:7], 0, v[70:71]
	v_lshl_add_u64 v[70:71], v[70:71], 0, v[134:135]
	s_waitcnt lgkmcnt(0)
	global_store_dwordx4 v[70:71], v[66:69], off nt
	s_nop 1
	v_or_b32_e32 v66, s4, v144
	v_or_b32_e32 v70, s33, v66
	ds_read_b128 v[66:69], v164
	v_ashrrev_i32_e32 v71, 31, v70
	v_lshlrev_b64 v[70:71], 10, v[70:71]
	v_lshl_add_u64 v[70:71], s[6:7], 0, v[70:71]
	v_lshl_add_u64 v[70:71], v[70:71], 0, v[134:135]
	s_waitcnt lgkmcnt(0)
	global_store_dwordx4 v[70:71], v[66:69], off nt
	s_nop 1
	v_or_b32_e32 v66, s4, v145
	v_or_b32_e32 v70, s33, v66
	ds_read_b128 v[66:69], v165
	v_ashrrev_i32_e32 v71, 31, v70
	v_lshlrev_b64 v[70:71], 10, v[70:71]
	v_lshl_add_u64 v[70:71], s[6:7], 0, v[70:71]
	v_lshl_add_u64 v[70:71], v[70:71], 0, v[134:135]
	s_waitcnt lgkmcnt(0)
	global_store_dwordx4 v[70:71], v[66:69], off nt
	s_nop 1
	v_or_b32_e32 v66, s4, v146
	v_or_b32_e32 v70, s33, v66
	ds_read_b128 v[66:69], v166
	v_ashrrev_i32_e32 v71, 31, v70
	v_lshlrev_b64 v[70:71], 10, v[70:71]
	v_lshl_add_u64 v[70:71], s[6:7], 0, v[70:71]
	v_lshl_add_u64 v[70:71], v[70:71], 0, v[134:135]
	s_waitcnt lgkmcnt(0)
	global_store_dwordx4 v[70:71], v[66:69], off nt
	s_nop 1
	v_or_b32_e32 v66, s4, v147
	v_or_b32_e32 v70, s33, v66
	ds_read_b128 v[66:69], v167
	v_ashrrev_i32_e32 v71, 31, v70
	v_lshlrev_b64 v[70:71], 10, v[70:71]
	v_lshl_add_u64 v[70:71], s[6:7], 0, v[70:71]
	v_lshl_add_u64 v[70:71], v[70:71], 0, v[134:135]
	s_waitcnt lgkmcnt(0)
	global_store_dwordx4 v[70:71], v[66:69], off nt
	s_nop 1
	v_or_b32_e32 v66, s4, v148
	v_or_b32_e32 v70, s33, v66
	ds_read_b128 v[66:69], v168
	v_ashrrev_i32_e32 v71, 31, v70
	v_lshlrev_b64 v[70:71], 10, v[70:71]
	v_lshl_add_u64 v[70:71], s[6:7], 0, v[70:71]
	v_lshl_add_u64 v[70:71], v[70:71], 0, v[134:135]
	s_waitcnt lgkmcnt(0)
	global_store_dwordx4 v[70:71], v[66:69], off nt
	s_nop 1
	v_or_b32_e32 v66, s4, v149
	v_or_b32_e32 v70, s33, v66
	ds_read_b128 v[66:69], v169
	v_ashrrev_i32_e32 v71, 31, v70
	v_lshlrev_b64 v[70:71], 10, v[70:71]
	v_lshl_add_u64 v[70:71], s[6:7], 0, v[70:71]
	v_lshl_add_u64 v[70:71], v[70:71], 0, v[134:135]
	s_waitcnt lgkmcnt(0)
	global_store_dwordx4 v[70:71], v[66:69], off nt
	s_nop 1
	v_or_b32_e32 v66, s4, v150
	v_or_b32_e32 v70, s33, v66
	ds_read_b128 v[66:69], v170
	v_ashrrev_i32_e32 v71, 31, v70
	v_lshlrev_b64 v[70:71], 10, v[70:71]
	v_lshl_add_u64 v[70:71], s[6:7], 0, v[70:71]
	v_lshl_add_u64 v[70:71], v[70:71], 0, v[134:135]
	s_waitcnt lgkmcnt(0)
	global_store_dwordx4 v[70:71], v[66:69], off nt
	s_nop 1
	v_or_b32_e32 v66, s4, v151
	v_or_b32_e32 v70, s33, v66
	ds_read_b128 v[66:69], v171
	v_ashrrev_i32_e32 v71, 31, v70
	v_lshlrev_b64 v[70:71], 10, v[70:71]
	v_lshl_add_u64 v[70:71], s[6:7], 0, v[70:71]
	v_lshl_add_u64 v[70:71], v[70:71], 0, v[134:135]
	s_waitcnt lgkmcnt(0)
	global_store_dwordx4 v[70:71], v[66:69], off nt
	s_nop 1
	v_or_b32_e32 v66, s4, v152
	v_or_b32_e32 v70, s33, v66
	ds_read_b128 v[66:69], v172
	v_ashrrev_i32_e32 v71, 31, v70
	v_lshlrev_b64 v[70:71], 10, v[70:71]
	v_lshl_add_u64 v[70:71], s[6:7], 0, v[70:71]
	v_lshl_add_u64 v[70:71], v[70:71], 0, v[134:135]
	s_waitcnt lgkmcnt(0)
	global_store_dwordx4 v[70:71], v[66:69], off nt
	s_nop 1
	v_or_b32_e32 v66, s4, v153
	v_or_b32_e32 v70, s33, v66
	ds_read_b128 v[66:69], v173
	v_ashrrev_i32_e32 v71, 31, v70
	v_lshlrev_b64 v[70:71], 10, v[70:71]
	v_lshl_add_u64 v[70:71], s[6:7], 0, v[70:71]
	v_lshl_add_u64 v[70:71], v[70:71], 0, v[134:135]
	s_waitcnt lgkmcnt(0)
	global_store_dwordx4 v[70:71], v[66:69], off nt
	s_nop 1
	v_or_b32_e32 v66, s4, v154
	v_or_b32_e32 v70, s33, v66
	ds_read_b128 v[66:69], v174
	v_ashrrev_i32_e32 v71, 31, v70
	v_lshlrev_b64 v[70:71], 10, v[70:71]
	v_lshl_add_u64 v[70:71], s[6:7], 0, v[70:71]
	v_lshl_add_u64 v[70:71], v[70:71], 0, v[134:135]
	s_waitcnt lgkmcnt(0)
	global_store_dwordx4 v[70:71], v[66:69], off nt
	s_nop 1
	v_or_b32_e32 v66, s4, v155
	v_or_b32_e32 v70, s33, v66
	ds_read_b128 v[66:69], v175
	v_ashrrev_i32_e32 v71, 31, v70
	v_lshlrev_b64 v[70:71], 10, v[70:71]
	v_lshl_add_u64 v[70:71], s[6:7], 0, v[70:71]
	v_lshl_add_u64 v[70:71], v[70:71], 0, v[134:135]
	s_waitcnt lgkmcnt(0)
	global_store_dwordx4 v[70:71], v[66:69], off nt
	s_waitcnt lgkmcnt(0)
	s_add_i32 s4, s2, 0xfffffe00
	s_cmpk_lt_i32 s4, 0x510
	s_mov_b64 s[6:7], s[8:9]
	s_cbranch_scc0 .LBB0_1458

; __device__ __forceinline__ void unpack8(const v4u w, float (&y)[8]) { y[0] = bf_lo(w.x); y[1] = bf_hi(w.x); y[2] = bf_lo(w.y); y[3] = bf_hi(w.y); y[4] = bf_lo(w.z); y[5] = bf_hi(w.z); y[6] = bf_lo(w.w); y[7] = bf_hi(w.w); }
; __device__ __forceinline__ void combine_phase(bf16* x, const unsigned char* Y  , const int* SEL, const float* g, bf16* XN, float* fout, int gw, int NGW, int lane) {
;     ...
;         const int b = row0 >> 13, s0 = row0 & (SEQ - 1);
;         bf16* xr = x + (size_t)row0 * DM + 8 * lane;
;         v4u w0[R], w1[R]; int sel[R];
;         const int* selp = SEL + ((size_t)b * NE + (lane & 15)) * SEQ + s0;
; #pragma unroll
;         for (int r = 0; r < R; ++r) { w0[r] = *(const v4u*)(xr + (size_t)r * DM); w1[r] = *(const v4u*)(xr + (size_t)r * DM + 512); sel[r] = selp[r]; }
;         float a[R][16]; unsigned mk[R];
; #pragma unroll
;         for (int r = 0; r < R; ++r) { float t[8]; unpack8(w0[r], t);
; #pragma unroll
;             for (int i = 0; i < 8; ++i) a[r][i] = t[i];
;             unpack8(w1[r], t);
; #pragma unroll
;             for (int i = 0; i < 8; ++i) a[r][8 + i] = t[i];
;             mk[r] = (unsigned)__ballot(sel[r] >= 0) & 0xffffu; }
;         constexpr int NI = 3;
;         { v2u y0[NI][R], y1[NI][R];
; #pragma unroll
;           for (int it = 0; it < NI; ++it)
; #pragma unroll
;             for (int r = 0; r < R; ++r) {
;                 const bool h = mk[r] != 0u; const int e = h ? __builtin_ctz(mk[r]) : 0; const int sl = __builtin_amdgcn_readlane(sel[r], e); mk[r] &= mk[r] - 1u;
;                 y0[it][r] = (v2u){0u, 0u}; y1[it][r] = y0[it][r];
;                 if (h) { const unsigned char* yr = Y + (((size_t)e * NB + b) * CAP + sl) * DM + 8 * lane; y0[it][r] = *(const v2u*)yr; y1[it][r] = *(const v2u*)(yr + 512); }
;             }
.LBB0_1674:
	s_ashr_i32 s8, s0, 13
	s_ashr_i32 s9, s8, 31
	s_and_b32 s4, s0, 0x1ffc
	s_lshl_b64 s[12:13], s[8:9], 19
	v_lshl_add_u64 v[0:1], v[72:73], 0, s[12:13]
	s_lshl_b32 s4, s4, 2
	v_lshl_add_u64 v[0:1], v[0:1], 0, s[4:5]
	s_ashr_i32 s1, s0, 31
	global_load_dwordx4 v[0:3], v[0:1], off nt
	s_lshl_b64 s[10:11], s[0:1], 11
	v_lshl_add_u64 v[76:77], v[70:71], 0, s[10:11]
	v_add_co_u32_e32 v36, vcc, s20, v76
	global_load_dwordx4 v[32:35], v[76:77], off nt
	global_load_dwordx4 v[28:31], v[76:77], off offset:1024 nt
	global_load_dwordx4 v[24:27], v[76:77], off offset:2048 nt
	global_load_dwordx4 v[20:23], v[76:77], off offset:3072 nt
	v_addc_co_u32_e32 v37, vcc, 0, v77, vcc
	global_load_dwordx4 v[12:15], v[36:37], off offset:1024 nt
	global_load_dwordx4 v[8:11], v[36:37], off offset:2048 nt
	global_load_dwordx4 v[4:7], v[36:37], off offset:3072 nt
	global_load_dwordx4 v[16:19], v[36:37], off nt
	v_mov_b32_e32 v38, 0
	v_mov_b32_e32 v39, 0
	v_mov_b32_e32 v36, 0
	v_mov_b32_e32 v37, 0
	s_waitcnt vmcnt(8)
	v_cmp_lt_i32_e64 s[16:17], -1, v0
	v_cmp_lt_i32_e64 s[14:15], -1, v1
	s_and_b32 s15, s16, 0xffff
	s_cmp_eq_u32 s15, 0
	s_cselect_b64 s[18:19], -1, 0
	v_cmp_lt_i32_e64 s[10:11], -1, v3
	s_ff1_i32_b32 s4, s15
	s_and_b64 vcc, exec, s[18:19]
	s_cselect_b32 s11, 0, s4
	v_cmp_lt_i32_e64 s[12:13], -1, v2
	v_readlane_b32 s18, v0, s11
	s_cbranch_vccnz .LBB0_1676
	s_lshl_b32 s4, s4, 2
	s_add_u32 s22, s4, s8
	s_addc_u32 s23, 0, s9
	s_ashr_i32 s19, s18, 31
	s_lshl_b64 s[22:23], s[22:23], 20
	s_lshl_b64 s[18:19], s[18:19], 10
	s_add_u32 s4, s94, s22
	s_addc_u32 s11, s95, s23
	s_add_u32 s18, s4, s18
	s_addc_u32 s19, s11, s19
	v_lshl_add_u64 v[40:41], s[18:19], 0, v[68:69]
	global_load_dwordx2 v[38:39], v[40:41], off nt
	global_load_dwordx2 v[36:37], v[40:41], off offset:512 nt
.LBB0_1676:
	s_and_b32 s13, s14, 0xffff
	s_cmp_eq_u32 s13, 0
	s_cselect_b64 s[18:19], -1, 0
	s_ff1_i32_b32 s4, s13
	s_and_b64 vcc, s[18:19], exec
	s_cselect_b32 s11, 0, s4
	v_readlane_b32 s18, v1, s11
	v_mov_b32_e32 v40, 0
	v_mov_b32_e32 v44, 0
	v_mov_b32_e32 v45, 0
	v_mov_b32_e32 v42, 0
	v_mov_b32_e32 v43, 0
	s_cbranch_vccnz .LBB0_1678
	s_lshl_b32 s4, s4, 2
	s_add_u32 s22, s4, s8
	s_addc_u32 s23, 0, s9
	s_ashr_i32 s19, s18, 31
	s_lshl_b64 s[22:23], s[22:23], 20
	s_lshl_b64 s[18:19], s[18:19], 10
	s_add_u32 s4, s94, s22
	s_addc_u32 s11, s95, s23
	s_add_u32 s18, s4, s18
	s_addc_u32 s19, s11, s19
	v_lshl_add_u64 v[46:47], s[18:19], 0, v[68:69]
	global_load_dwordx2 v[44:45], v[46:47], off nt
	global_load_dwordx2 v[42:43], v[46:47], off offset:512 nt
.LBB0_1678:
	s_and_b32 s11, s12, 0xffff
	s_cmp_eq_u32 s11, 0
	s_cselect_b64 s[18:19], -1, 0
	s_ff1_i32_b32 s4, s11
	s_and_b64 vcc, s[18:19], exec
	s_cselect_b32 s17, 0, s4
	v_readlane_b32 s18, v2, s17
	v_mov_b32_e32 v41, 0
	v_mov_b32_e32 v46, 0
	v_mov_b32_e32 v47, 0
	s_cbranch_vccnz .LBB0_1680
	s_lshl_b32 s4, s4, 2
	s_add_u32 s22, s4, s8
	s_addc_u32 s23, 0, s9
	s_ashr_i32 s19, s18, 31
	s_lshl_b64 s[22:23], s[22:23], 20
	s_lshl_b64 s[18:19], s[18:19], 10
	s_add_u32 s4, s94, s22
	s_addc_u32 s17, s95, s23
	s_add_u32 s18, s4, s18
	s_addc_u32 s19, s17, s19
	v_lshl_add_u64 v[48:49], s[18:19], 0, v[68:69]
	global_load_dwordx2 v[40:41], v[48:49], off nt
	global_load_dwordx2 v[46:47], v[48:49], off offset:512 nt
.LBB0_1680:
	s_and_b32 s4, s10, 0xffff
	s_cmp_eq_u32 s4, 0
	s_cselect_b64 s[18:19], -1, 0
	s_ff1_i32_b32 s17, s4
	s_and_b64 vcc, s[18:19], exec
	s_cselect_b32 s18, 0, s17
	v_readlane_b32 s18, v3, s18
	v_mov_b32_e32 v48, 0
	v_mov_b32_e32 v52, 0
	v_mov_b32_e32 v53, 0
	v_mov_b32_e32 v50, 0
	v_mov_b32_e32 v51, 0
	s_cbranch_vccnz .LBB0_1682
	s_lshl_b32 s17, s17, 2
	s_add_u32 s22, s17, s8
	s_addc_u32 s23, 0, s9
	s_ashr_i32 s19, s18, 31
	s_lshl_b64 s[22:23], s[22:23], 20
	s_lshl_b64 s[18:19], s[18:19], 10
	s_add_u32 s17, s94, s22
	s_addc_u32 s21, s95, s23
	s_add_u32 s18, s17, s18
	s_addc_u32 s19, s21, s19
	v_lshl_add_u64 v[54:55], s[18:19], 0, v[68:69]
	global_load_dwordx2 v[52:53], v[54:55], off nt
	global_load_dwordx2 v[50:51], v[54:55], off offset:512 nt
.LBB0_1682:
	s_add_i32 s16, s16, -1
	s_and_b32 s18, s16, s15
	s_cmp_eq_u32 s18, 0
	s_cselect_b64 s[16:17], -1, 0
	s_ff1_i32_b32 s15, s18
	s_and_b64 vcc, s[16:17], exec
	s_cselect_b32 s16, 0, s15
	v_readlane_b32 s16, v0, s16
	v_mov_b32_e32 v49, 0
	v_mov_b32_e32 v54, 0
	v_mov_b32_e32 v55, 0
	s_cbranch_vccnz .LBB0_1684
	s_lshl_b32 s15, s15, 2
	s_add_u32 s22, s15, s8
	s_addc_u32 s23, 0, s9
	s_ashr_i32 s17, s16, 31
	s_lshl_b64 s[22:23], s[22:23], 20
	s_lshl_b64 s[16:17], s[16:17], 10
	s_add_u32 s15, s94, s22
	s_addc_u32 s19, s95, s23
	s_add_u32 s16, s15, s16
	s_addc_u32 s17, s19, s17
	v_lshl_add_u64 v[56:57], s[16:17], 0, v[68:69]
	global_load_dwordx2 v[48:49], v[56:57], off nt
	global_load_dwordx2 v[54:55], v[56:57], off offset:512 nt
; __device__ __forceinline__ void combine_phase(bf16* x, const unsigned char* Y  , const int* SEL, const float* g, bf16* XN, float* fout, int gw, int NGW, int lane) {
;     ...
;         { v2u y0[NI][R], y1[NI][R];
; #pragma unroll
;           for (int it = 0; it < NI; ++it)
; #pragma unroll
;             for (int r = 0; r < R; ++r) {
;                 const bool h = mk[r] != 0u; const int e = h ? __builtin_ctz(mk[r]) : 0; const int sl = __builtin_amdgcn_readlane(sel[r], e); mk[r] &= mk[r] - 1u;
;                 y0[it][r] = (v2u){0u, 0u}; y1[it][r] = y0[it][r];
;                 if (h) { const unsigned char* yr = Y + (((size_t)e * NB + b) * CAP + sl) * DM + 8 * lane; y0[it][r] = *(const v2u*)yr; y1[it][r] = *(const v2u*)(yr + 512); }
;             }
.LBB0_1684:
	s_add_i32 s14, s14, -1
	s_and_b32 s16, s14, s13
	s_cmp_eq_u32 s16, 0
	s_cselect_b64 s[14:15], -1, 0
	s_ff1_i32_b32 s13, s16
	s_and_b64 vcc, s[14:15], exec
	s_cselect_b32 s14, 0, s13
	v_readlane_b32 s14, v1, s14
	v_mov_b32_e32 v56, 0
	v_mov_b32_e32 v60, 0
	v_mov_b32_e32 v61, 0
	v_mov_b32_e32 v58, 0
	v_mov_b32_e32 v59, 0
	s_cbranch_vccnz .LBB0_1686
	s_lshl_b32 s13, s13, 2
	s_add_u32 s22, s13, s8
	s_addc_u32 s23, 0, s9
	s_ashr_i32 s15, s14, 31
	s_lshl_b64 s[22:23], s[22:23], 20
	s_lshl_b64 s[14:15], s[14:15], 10
	s_add_u32 s13, s94, s22
	s_addc_u32 s17, s95, s23
	s_add_u32 s14, s13, s14
	s_addc_u32 s15, s17, s15
	v_lshl_add_u64 v[62:63], s[14:15], 0, v[68:69]
	global_load_dwordx2 v[60:61], v[62:63], off nt
	global_load_dwordx2 v[58:59], v[62:63], off offset:512 nt
.LBB0_1686:
	s_add_i32 s12, s12, -1
	s_and_b32 s15, s12, s11
	s_cmp_eq_u32 s15, 0
	s_cselect_b64 s[12:13], -1, 0
	s_ff1_i32_b32 s11, s15
	s_and_b64 vcc, s[12:13], exec
	s_cselect_b32 s12, 0, s11
	v_readlane_b32 s12, v2, s12
	v_mov_b32_e32 v57, 0
	v_mov_b32_e32 v62, 0
	v_mov_b32_e32 v63, 0
	s_cbranch_vccnz .LBB0_1688
	s_lshl_b32 s11, s11, 2
	s_add_u32 s22, s11, s8
	s_addc_u32 s23, 0, s9
	s_ashr_i32 s13, s12, 31
	s_lshl_b64 s[22:23], s[22:23], 20
	s_lshl_b64 s[12:13], s[12:13], 10
	s_add_u32 s11, s94, s22
	s_addc_u32 s14, s95, s23
	s_add_u32 s12, s11, s12
	s_addc_u32 s13, s14, s13
	v_lshl_add_u64 v[64:65], s[12:13], 0, v[68:69]
	global_load_dwordx2 v[56:57], v[64:65], off nt
	global_load_dwordx2 v[62:63], v[64:65], off offset:512 nt
.LBB0_1688:
	s_add_i32 s10, s10, -1
	s_and_b32 s4, s10, s4
	s_cmp_eq_u32 s4, 0
	s_cselect_b64 s[12:13], -1, 0
	s_ff1_i32_b32 s11, s4
	s_and_b64 vcc, s[12:13], exec
	s_cselect_b32 s10, 0, s11
	v_readlane_b32 s10, v3, s10
	v_mov_b32_e32 v64, 0
	v_mov_b32_e32 v78, 0
	v_mov_b32_e32 v79, 0
	v_mov_b32_e32 v66, 0
	v_mov_b32_e32 v67, 0
	s_cbranch_vccnz .LBB0_1690
	s_lshl_b32 s11, s11, 2
	s_add_u32 s12, s11, s8
	s_addc_u32 s13, 0, s9
	s_ashr_i32 s11, s10, 31
	s_lshl_b64 s[12:13], s[12:13], 20
	s_lshl_b64 s[10:11], s[10:11], 10
	s_add_u32 s12, s94, s12
	s_addc_u32 s13, s95, s13
	s_add_u32 s10, s12, s10
	s_addc_u32 s11, s13, s11
	v_lshl_add_u64 v[80:81], s[10:11], 0, v[68:69]
	global_load_dwordx2 v[78:79], v[80:81], off nt
	global_load_dwordx2 v[66:67], v[80:81], off offset:512 nt
.LBB0_1690:
	s_add_i32 s10, s18, -1
	s_and_b32 s14, s10, s18
	s_cmp_eq_u32 s14, 0
	s_cselect_b64 s[12:13], -1, 0
	s_ff1_i32_b32 s11, s14
	s_and_b64 vcc, s[12:13], exec
	s_cselect_b32 s10, 0, s11
	v_readlane_b32 s10, v0, s10
	v_mov_b32_e32 v65, 0
	v_mov_b32_e32 v82, 0
	v_mov_b32_e32 v83, 0
	s_cbranch_vccnz .LBB0_1692
	s_lshl_b32 s11, s11, 2
	s_add_u32 s12, s11, s8
	s_addc_u32 s13, 0, s9
	s_ashr_i32 s11, s10, 31
	s_lshl_b64 s[12:13], s[12:13], 20
	s_lshl_b64 s[10:11], s[10:11], 10
	s_add_u32 s12, s94, s12
	s_addc_u32 s13, s95, s13
	s_add_u32 s10, s12, s10
	s_addc_u32 s11, s13, s11
	v_lshl_add_u64 v[80:81], s[10:11], 0, v[68:69]
	global_load_dwordx2 v[64:65], v[80:81], off nt
	global_load_dwordx2 v[82:83], v[80:81], off offset:512 nt
.LBB0_1692:
	s_add_i32 s10, s16, -1
	s_and_b32 s13, s10, s16
	s_cmp_eq_u32 s13, 0
	s_cselect_b64 s[16:17], -1, 0
	s_ff1_i32_b32 s11, s13
	s_and_b64 vcc, s[16:17], exec
	s_cselect_b32 s10, 0, s11
	v_readlane_b32 s10, v1, s10
	v_mov_b32_e32 v80, 0
	v_mov_b32_e32 v86, 0
	v_mov_b32_e32 v87, 0
	v_mov_b32_e32 v84, 0
	v_mov_b32_e32 v85, 0
	s_cbranch_vccnz .LBB0_1694
	s_lshl_b32 s11, s11, 2
	s_add_u32 s16, s11, s8
	s_addc_u32 s17, 0, s9
	s_ashr_i32 s11, s10, 31
	s_lshl_b64 s[16:17], s[16:17], 20
	s_lshl_b64 s[10:11], s[10:11], 10
	s_add_u32 s12, s94, s16
	s_addc_u32 s16, s95, s17
	s_add_u32 s10, s12, s10
	s_addc_u32 s11, s16, s11
	v_lshl_add_u64 v[88:89], s[10:11], 0, v[68:69]
	global_load_dwordx2 v[86:87], v[88:89], off nt
	global_load_dwordx2 v[84:85], v[88:89], off offset:512 nt
.LBB0_1694:
	s_add_i32 s10, s15, -1
	s_and_b32 s12, s10, s15
	s_cmp_eq_u32 s12, 0
	s_cselect_b64 s[16:17], -1, 0
	s_ff1_i32_b32 s11, s12
	s_and_b64 vcc, s[16:17], exec
	s_cselect_b32 s10, 0, s11
	v_readlane_b32 s10, v2, s10
	v_mov_b32_e32 v81, 0
	v_mov_b32_e32 v88, 0
	v_mov_b32_e32 v89, 0
	s_cbranch_vccnz .LBB0_1696
	s_lshl_b32 s11, s11, 2
	s_add_u32 s16, s11, s8
	s_addc_u32 s17, 0, s9
	s_ashr_i32 s11, s10, 31
	s_lshl_b64 s[16:17], s[16:17], 20
	s_lshl_b64 s[10:11], s[10:11], 10
	s_add_u32 s15, s94, s16
	s_addc_u32 s16, s95, s17
	s_add_u32 s10, s15, s10
	s_addc_u32 s11, s16, s11
	v_lshl_add_u64 v[90:91], s[10:11], 0, v[68:69]
	global_load_dwordx2 v[80:81], v[90:91], off nt
	global_load_dwordx2 v[88:89], v[90:91], off offset:512 nt
.LBB0_1696:
	s_add_i32 s10, s4, -1
	s_and_b32 s4, s10, s4
	s_cmp_eq_u32 s4, 0
	s_cselect_b64 s[16:17], -1, 0
	s_ff1_i32_b32 s11, s4
	s_and_b64 vcc, s[16:17], exec
	s_cselect_b32 s10, 0, s11
	v_readlane_b32 s10, v3, s10
	v_mov_b32_e32 v92, 0
	v_mov_b32_e32 v93, 0
	v_mov_b32_e32 v90, 0
	v_mov_b32_e32 v91, 0
	s_cbranch_vccnz .LBB0_1698
	s_lshl_b32 s11, s11, 2
	s_add_u32 s16, s11, s8
	s_addc_u32 s17, 0, s9
	s_ashr_i32 s11, s10, 31
	s_lshl_b64 s[16:17], s[16:17], 20
	s_lshl_b64 s[10:11], s[10:11], 10
	s_add_u32 s15, s94, s16
	s_addc_u32 s16, s95, s17
	s_add_u32 s10, s15, s10
	s_addc_u32 s11, s16, s11
	v_lshl_add_u64 v[94:95], s[10:11], 0, v[68:69]
	global_load_dwordx2 v[92:93], v[94:95], off nt
	global_load_dwordx2 v[90:91], v[94:95], off offset:512 nt

; __device__ __forceinline__ void combine_phase(bf16* x, const unsigned char* Y  , const int* SEL, const float* g, bf16* XN, float* fout, int gw, int NGW, int lane) {
;     ...
; #pragma unroll
;         for (int r = 0; r < R; ++r) {
;             float (&v)[16] = a[r]; const int row = row0 + r;
;             if (fout) { float* o = fout + (size_t)row * DM + 8 * lane;
;                 *(f32x4*)o = (f32x4){v[0], v[1], v[2], v[3]}; *(f32x4*)(o + 4) = (f32x4){v[4], v[5], v[6], v[7]}; *(f32x4*)(o + 512) = (f32x4){v[8], v[9], v[10], v[11]}; *(f32x4*)(o + 516) = (f32x4){v[12], v[13], v[14], v[15]}; }
.LBB0_1699:
	s_and_b64 vcc, exec, s[2:3]
	s_cbranch_vccz .LBB0_1673
	s_lshl_b64 s[8:9], s[0:1], 12
	v_lshl_add_u64 v[0:1], v[74:75], 0, s[8:9]
	s_or_b32 s8, s0, 1
	s_ashr_i32 s9, s8, 31
	s_lshl_b64 s[8:9], s[8:9], 12
	global_store_dwordx4 v[0:1], v[16:19], off nt
	global_store_dwordx4 v[0:1], v[12:15], off offset:16 nt
	global_store_dwordx4 v[0:1], v[8:11], off offset:2048 nt
	global_store_dwordx4 v[0:1], v[4:7], off offset:2064 nt
	v_lshl_add_u64 v[0:1], v[74:75], 0, s[8:9]
	s_or_b32 s8, s0, 2
	s_ashr_i32 s9, s8, 31
	s_lshl_b64 s[8:9], s[8:9], 12
	global_store_dwordx4 v[0:1], v[20:23], off nt
	global_store_dwordx4 v[0:1], v[24:27], off offset:16 nt
	global_store_dwordx4 v[0:1], v[32:35], off offset:2048 nt
	global_store_dwordx4 v[0:1], v[40:43], off offset:2064 nt
	v_lshl_add_u64 v[0:1], v[74:75], 0, s[8:9]
	s_or_b32 s8, s0, 3
	s_ashr_i32 s9, s8, 31
	s_lshl_b64 s[8:9], s[8:9], 12
	s_add_i32 s0, s0, s7
	s_cmpk_gt_i32 s0, 0x7fff
	global_store_dwordx4 v[0:1], v[28:31], off nt
	global_store_dwordx4 v[0:1], v[36:39], off offset:16 nt
	global_store_dwordx4 v[0:1], v[48:51], off offset:2048 nt
	global_store_dwordx4 v[0:1], v[56:59], off offset:2064 nt
	v_lshl_add_u64 v[0:1], v[74:75], 0, s[8:9]
	s_mov_b64 s[8:9], 0
	s_cselect_b64 s[10:11], -1, 0
	global_store_dwordx4 v[0:1], v[44:47], off nt
	global_store_dwordx4 v[0:1], v[52:55], off offset:16 nt
	global_store_dwordx4 v[0:1], v[60:63], off offset:2048 nt
	global_store_dwordx4 v[0:1], v[64:67], off offset:2064 nt
	s_andn2_b64 vcc, exec, s[10:11]
	s_cbranch_vccnz .LBB0_1674
	s_branch .LBB0_1710

; __device__ __forceinline__ v4u pack8(const float (&y)[8]) { v4u w; w.x = pkbf(y[0], y[1]); w.y = pkbf(y[2], y[3]); w.z = pkbf(y[4], y[5]); w.w = pkbf(y[6], y[7]); return w; }
; __device__ __forceinline__ void combine_phase(bf16* x, const unsigned char* Y  , const int* SEL, const float* g, bf16* XN, float* fout, int gw, int NGW, int lane) {
;     ...
;         while (mk[0] | mk[1] | mk[2] | mk[3]) {
;             v2u y0[R], y1[R];
; #pragma unroll
;             for (int r = 0; r < R; ++r) {
;                 const bool h = mk[r] != 0u; const int e = h ? __builtin_ctz(mk[r]) : 0; const int sl = __builtin_amdgcn_readlane(sel[r], e); mk[r] &= mk[r] - 1u;
;                 y0[r] = (v2u){0u, 0u}; y1[r] = y0[r];
;                 if (h) { const unsigned char* yr = Y + (((size_t)e * NB + b) * CAP + sl) * DM + 8 * lane; y0[r] = *(const v2u*)yr; y1[r] = *(const v2u*)(yr + 512); }
;             }
;     ...
;             else {
;                 bf16* xo = x + (size_t)row * DM + 8 * lane;
;                 { float t[8];
; #pragma unroll
;                   for (int i = 0; i < 8; ++i) t[i] = v[i];
;                   *(v4u*)xo = pack8(t);
.LBB0_1702:
	v_sub_co_u32_e64 v78, s[16:17], s14, 1
	s_ff1_i32_b32 s11, s14
	s_and_b64 vcc, s[16:17], exec
	s_cselect_b32 s10, 0, s11
	v_readfirstlane_b32 s15, v78
	v_readlane_b32 s10, v0, s10
	v_mov_b32_e32 v78, 0
	v_mov_b32_e32 v82, 0
	v_mov_b32_e32 v83, 0
	v_mov_b32_e32 v80, 0
	v_mov_b32_e32 v81, 0
	s_cbranch_vccnz .LBB0_1704
	s_lshl_b32 s11, s11, 2
	s_add_u32 s16, s11, s8
	s_addc_u32 s17, 0, s9
	s_ashr_i32 s11, s10, 31
	s_lshl_b64 s[16:17], s[16:17], 20
	s_lshl_b64 s[10:11], s[10:11], 10
	s_add_u32 s16, s94, s16
	s_addc_u32 s17, s95, s17
	s_add_u32 s10, s16, s10
	s_addc_u32 s11, s17, s11
	v_lshl_add_u64 v[84:85], s[10:11], 0, v[68:69]
	global_load_dwordx2 v[82:83], v[84:85], off nt
	global_load_dwordx2 v[80:81], v[84:85], off offset:512 nt
.LBB0_1704:
	v_sub_co_u32_e64 v79, s[18:19], s13, 1
	s_ff1_i32_b32 s11, s13
	s_and_b64 vcc, s[18:19], exec
	s_cselect_b32 s10, 0, s11
	v_readfirstlane_b32 s16, v79
	v_readlane_b32 s10, v1, s10
	v_mov_b32_e32 v79, 0
	v_mov_b32_e32 v84, 0
	v_mov_b32_e32 v85, 0
	s_cbranch_vccnz .LBB0_1706
	s_lshl_b32 s11, s11, 2
	s_add_u32 s18, s11, s8
	s_addc_u32 s19, 0, s9
	s_ashr_i32 s11, s10, 31
	s_lshl_b64 s[18:19], s[18:19], 20
	s_lshl_b64 s[10:11], s[10:11], 10
	s_add_u32 s17, s94, s18
	s_addc_u32 s18, s95, s19
	s_add_u32 s10, s17, s10
	s_addc_u32 s11, s18, s11
	v_lshl_add_u64 v[86:87], s[10:11], 0, v[68:69]
	global_load_dwordx2 v[78:79], v[86:87], off nt
	global_load_dwordx2 v[84:85], v[86:87], off offset:512 nt
.LBB0_1706:
	v_sub_co_u32_e64 v86, s[18:19], s12, 1
	s_ff1_i32_b32 s11, s12
	s_and_b64 vcc, s[18:19], exec
	s_cselect_b32 s10, 0, s11
	v_readfirstlane_b32 s17, v86
	v_readlane_b32 s10, v2, s10
	v_mov_b32_e32 v86, 0
	v_mov_b32_e32 v90, 0
	v_mov_b32_e32 v91, 0
	v_mov_b32_e32 v88, 0
	v_mov_b32_e32 v89, 0
	s_cbranch_vccnz .LBB0_1708
	s_lshl_b32 s11, s11, 2
	s_add_u32 s18, s11, s8
	s_addc_u32 s19, 0, s9
	s_ashr_i32 s11, s10, 31
	s_lshl_b64 s[18:19], s[18:19], 20
	s_lshl_b64 s[10:11], s[10:11], 10
	s_add_u32 s18, s94, s18
	s_addc_u32 s19, s95, s19
	s_add_u32 s10, s18, s10
	s_addc_u32 s11, s19, s11
	v_lshl_add_u64 v[92:93], s[10:11], 0, v[68:69]
	global_load_dwordx2 v[90:91], v[92:93], off nt
	global_load_dwordx2 v[88:89], v[92:93], off offset:512 nt
.LBB0_1708:
	v_sub_co_u32_e64 v87, s[22:23], s4, 1
	s_ff1_i32_b32 s11, s4
	s_and_b64 vcc, s[22:23], exec
	s_cselect_b32 s10, 0, s11
	v_readfirstlane_b32 s18, v87
	v_readlane_b32 s10, v3, s10
	v_mov_b32_e32 v87, 0
	v_mov_b32_e32 v92, 0
	v_mov_b32_e32 v93, 0
	s_cbranch_vccnz .LBB0_1701
	s_lshl_b32 s11, s11, 2
	s_add_u32 s22, s11, s8
	s_addc_u32 s23, 0, s9
	s_ashr_i32 s11, s10, 31
	s_lshl_b64 s[22:23], s[22:23], 20
	s_lshl_b64 s[10:11], s[10:11], 10
	s_add_u32 s19, s94, s22
	s_addc_u32 s21, s95, s23
	s_add_u32 s10, s19, s10
	s_addc_u32 s11, s21, s11
	v_lshl_add_u64 v[94:95], s[10:11], 0, v[68:69]
	global_load_dwordx2 v[86:87], v[94:95], off nt
	global_load_dwordx2 v[92:93], v[94:95], off offset:512 nt
	s_branch .LBB0_1701
.LBB0_1710:
	s_and_b64 vcc, exec, s[8:9]
	s_cbranch_vccz .LBB0_1712
	v_cvt_pk_bf16_f32 v0, v16, v17
	v_cvt_pk_bf16_f32 v1, v18, v19
	v_cvt_pk_bf16_f32 v2, v12, v13
	v_cvt_pk_bf16_f32 v3, v14, v15
	global_store_dwordx4 v[76:77], v[0:3], off nt
	s_nop 1
	v_cvt_pk_bf16_f32 v0, v8, v9
	s_nop 0
	v_cvt_pk_bf16_f32 v0, v10, v11
	s_nop 0
	v_cvt_pk_bf16_f32 v0, v4, v5
	s_nop 0
	v_cvt_pk_bf16_f32 v0, v6, v7
